# stack of validated edits: nt/sc1 cache hints (P0, GEMM3 epilogue), GEMM3 epilogue loads pipelined, P9a gather issue order + waits, hook chunks to VGPRs, P9b s_nop removal
# baseline (speedup 1.0000x reference)
; __device__ __forceinline__ unsigned cvt_pk_bf16(float lo, float hi) { unsigned r; asm volatile("v_cvt_pk_bf16_f32 %0, %1, %2" : "=v"(r) : "v"(lo), "v"(hi)); return r; }
;     __device__ __forceinline__ void operator()(const f32x4 (&acc)[2][2][4][2], const Unit& u, int wr, int wc, int fr, int fq) const {
;         const int row0 = u.pm * BM + wr * 64 + fr, col0 = u.pn * BM + wc * 32 + 8 * fq;
;         typedef unsigned u32x2e __attribute__((ext_vector_type(2)));
;         f32x4 gv[2][2];
; #pragma unroll
;         for (int bj = 0; bj < 2; ++bj)
; #pragma unroll
;             for (int n = 0; n < 2; ++n) gv[bj][n] = *(const f32x4*)(gain + col0 + bj * HALF + 4 * n);
;         float* SSQP = (float*)(ws + OFF_SSQP); unsigned char* Q8 = ws + OFF_Q8;
; #pragma unroll
;         for (int ai = 0; ai < 2; ++ai)
; #pragma unroll
;             for (int m = 0; m < 4; ++m) { const size_t r = (size_t)(row0 + ai * HALF + m * 16); float ss = 0.f;
; #pragma unroll
;                 for (int bj = 0; bj < 2; ++bj) { const size_t off = r * 4096 + col0 + bj * HALF;
;                     const f32x4 v0 = acc[ai][bj][m][0] * scale + *(const f32x4*)(R + off), v1 = acc[ai][bj][m][1] * scale + *(const f32x4*)(R + off + 4);
;                     ss += (v0[0] * v0[0] + v0[1] * v0[1]) + (v0[2] * v0[2] + v0[3] * v0[3]) + (v1[0] * v1[0] + v1[1] * v1[1]) + (v1[2] * v1[2] + v1[3] * v1[3]);
;                     u32x4 w; w.x = cvt_pk_bf16(v0[0], v0[1]); w.y = cvt_pk_bf16(v0[2], v0[3]); w.z = cvt_pk_bf16(v1[0], v1[1]); w.w = cvt_pk_bf16(v1[2], v1[3]);
;                     *(u32x4*)(HB + off) = w;
;                     u32x2e q; q.x = q8x4(v0, gv[bj][0], (float)HQS); q.y = q8x4(v1, gv[bj][1], (float)HQS);
;                     *(u32x2e*)(Q8 + r * LDQ8 + col0 + bj * HALF) = q; }
;                 ss += __shfl_xor(ss, 16); ss += __shfl_xor(ss, 32);
;                 if (fq == 0) SSQP[r * 64 + u.pn * 4 + wc] = ss; }
.LBB0_617:
	v_lshl_add_u32 v140, s29, 8, v169
	v_lshl_or_b32 v138, s28, 8, v170
	v_ashrrev_i32_e32 v141, 31, v140
	v_ashrrev_i32_e32 v139, 31, v138
	v_lshlrev_b64 v[66:67], 12, v[140:141]
	v_lshl_add_u64 v[154:155], v[66:67], 0, v[138:139]
	v_lshl_add_u64 v[156:157], v[154:155], 2, s[8:9]
	global_load_dwordx4 v[146:149], v[156:157], off nt
	global_load_dwordx4 v[150:153], v[156:157], off offset:16 nt
	v_lshlrev_b32_e32 v252, 2, v154
	global_load_dwordx4 v[244:247], v252, s[8:9] offset:512 nt
	global_load_dwordx4 v[248:251], v252, s[8:9] offset:528 nt
	v_lshl_add_u64 v[144:145], v[138:139], 2, s[52:53]
	global_load_dwordx4 v[74:77], v[144:145], off
	global_load_dwordx4 v[66:69], v[144:145], off offset:16
	v_cvt_f32_i32_e32 v159, v63
	v_cvt_f32_i32_e32 v158, v62
	v_cvt_f32_i32_e32 v161, v65
	v_cvt_f32_i32_e32 v160, v64
	v_cvt_f32_i32_e32 v179, v51
	v_cvt_f32_i32_e32 v178, v50
	v_cvt_f32_i32_e32 v181, v53
	v_cvt_f32_i32_e32 v180, v52
	v_lshlrev_b64 v[154:155], 1, v[154:155]
	global_load_dwordx4 v[50:53], v[144:145], off offset:528
	global_load_dwordx4 v[62:65], v[144:145], off offset:512
	s_add_u32 s98, s8, 0x40000
	s_addc_u32 s99, s9, 0
	global_load_dwordx4 v[212:215], v252, s[98:99] nt
	global_load_dwordx4 v[216:219], v252, s[98:99] offset:16 nt
	global_load_dwordx4 v[220:223], v252, s[98:99] offset:512 nt
	global_load_dwordx4 v[224:227], v252, s[98:99] offset:528 nt
	v_lshl_add_u64 v[182:183], s[14:15], 0, v[154:155]
	v_readlane_b32 s22, v255, 13
	v_readlane_b32 s23, v255, 14
	v_cvt_f32_i32_e32 v135, v135
	v_cvt_f32_i32_e32 v134, v134
	v_lshl_add_u64 v[142:143], s[22:23], 0, v[138:139]
	v_mad_i64_i32 v[144:145], s[22:23], v140, s50, v[142:143]
	v_cvt_f32_i32_e32 v137, v137
	v_cvt_f32_i32_e32 v136, v136
	v_cvt_f32_i32_e32 v131, v131
	v_cvt_f32_i32_e32 v130, v130
	v_or_b32_e32 v154, 0x100, v154
	v_lshl_add_u64 v[154:155], s[14:15], 0, v[154:155]
	s_lshl_b32 s22, s28, 2
	s_ashr_i32 s23, s22, 31
	s_lshl_b64 s[22:23], s[22:23], 2
	s_add_u32 s22, s48, s22
	s_addc_u32 s23, s49, s23
	s_waitcnt vmcnt(11)
	v_pk_fma_f32 v[160:161], v[160:161], s[26:27], v[148:149] op_sel_hi:[1,0,1]
	v_pk_fma_f32 v[158:159], v[158:159], s[26:27], v[146:147] op_sel_hi:[1,0,1]
	s_waitcnt vmcnt(10)
	v_pk_fma_f32 v[180:181], v[180:181], s[26:27], v[152:153] op_sel_hi:[1,0,1]
	v_pk_fma_f32 v[178:179], v[178:179], s[26:27], v[150:151] op_sel_hi:[1,0,1]
	v_cvt_pk_bf16_f32 v146, v158, v159
	v_cvt_pk_bf16_f32 v147, v160, v161
	s_waitcnt vmcnt(7)
	v_mul_f32_e32 v150, v74, v158
	v_cvt_pk_bf16_f32 v148, v178, v179
	v_cvt_pk_bf16_f32 v149, v180, v181
	v_mul_f32_e32 v151, v75, v159
	v_mul_f32_e32 v152, v76, v160
	v_mul_f32_e32 v153, v77, v161
	s_waitcnt vmcnt(6)
	v_mul_f32_e32 v184, v66, v178
	v_mul_f32_e32 v185, v67, v179
	v_mul_f32_e32 v186, v68, v180
	v_mul_f32_e32 v187, v69, v181
	global_store_dwordx4 v[182:183], v[146:149], off
	v_mul_f32_e32 v159, v159, v159
	v_mul_f32_e32 v161, v161, v161
	v_mul_f32_e32 v146, 0x41c00000, v150
	v_mul_f32_e32 v147, 0x41c00000, v151
	v_mul_f32_e32 v148, 0x41c00000, v152
	v_mul_f32_e32 v149, 0x41c00000, v153
	v_mul_f32_e32 v150, 0x41c00000, v184
	v_mul_f32_e32 v151, 0x41c00000, v185
	v_mul_f32_e32 v152, 0x41c00000, v186
	v_mul_f32_e32 v153, 0x41c00000, v187
	v_med3_f32 v146, v146, s51, v177
	v_med3_f32 v147, v147, s51, v177
	v_med3_f32 v148, v148, s51, v177
	v_med3_f32 v149, v149, s51, v177
	v_med3_f32 v150, v150, s51, v177
	v_med3_f32 v151, v151, s51, v177
	v_med3_f32 v152, v152, s51, v177
	v_med3_f32 v153, v153, s51, v177
	v_add_f32_e32 v146, 0x4b400000, v146
	v_add_f32_e32 v147, 0x4b400000, v147
	v_add_f32_e32 v148, 0x4b400000, v148
	v_add_f32_e32 v149, 0x4b400000, v149
	v_add_f32_e32 v150, 0x4b400000, v150
	v_add_f32_e32 v151, 0x4b400000, v151
	v_add_f32_e32 v152, 0x4b400000, v152
	v_add_f32_e32 v153, 0x4b400000, v153
	v_perm_b32 v146, v147, v146, s56
	v_perm_b32 v147, v149, v148, s57
	v_perm_b32 v148, v151, v150, s56
	v_perm_b32 v149, v153, v152, s57
	v_or_b32_e32 v146, v146, v147
	v_or_b32_e32 v147, v148, v149
	global_store_dwordx2 v[144:145], v[146:147], off
	s_nop 0
	s_nop 0
	s_nop 0
	v_cvt_f32_i32_e32 v157, v133
	v_cvt_f32_i32_e32 v156, v132
	v_and_b32_e32 v133, 64, v176
	v_mul_f32_e32 v179, v179, v179
	v_fmac_f32_e32 v159, v158, v158
	v_fmac_f32_e32 v161, v160, v160
	v_xor_b32_e32 v132, 16, v176
	v_add_u32_e32 v133, 64, v133
	v_mul_f32_e32 v181, v181, v181
	v_fmac_f32_e32 v179, v178, v178
	v_add_f32_e32 v158, v159, v161
	v_cmp_lt_i32_e32 vcc, v132, v133
	v_fmac_f32_e32 v181, v180, v180
	v_add_f32_e32 v158, v158, v179
	v_cndmask_b32_e32 v132, v176, v132, vcc
	v_add_f32_e32 v158, v181, v158
	v_lshlrev_b32_e32 v132, 2, v132
	v_xor_b32_e32 v182, 32, v176
	v_cmp_lt_i32_e32 vcc, v182, v133
	s_waitcnt vmcnt(6)
	v_pk_fma_f32 v[148:149], v[136:137], s[26:27], v[246:247] op_sel_hi:[1,0,1]
	v_pk_fma_f32 v[146:147], v[134:135], s[26:27], v[244:245] op_sel_hi:[1,0,1]
	s_waitcnt vmcnt(6)
; __device__ __forceinline__ unsigned cvt_pk_bf16(float lo, float hi) { unsigned r; asm volatile("v_cvt_pk_bf16_f32 %0, %1, %2" : "=v"(r) : "v"(lo), "v"(hi)); return r; }
;     __device__ __forceinline__ void operator()(const f32x4 (&acc)[2][2][4][2], const Unit& u, int wr, int wc, int fr, int fq) const {
;     ...
;             for (int m = 0; m < 4; ++m) { const size_t r = (size_t)(row0 + ai * HALF + m * 16); float ss = 0.f;
; #pragma unroll
;                 for (int bj = 0; bj < 2; ++bj) { const size_t off = r * 4096 + col0 + bj * HALF;
;                     const f32x4 v0 = acc[ai][bj][m][0] * scale + *(const f32x4*)(R + off), v1 = acc[ai][bj][m][1] * scale + *(const f32x4*)(R + off + 4);
;                     ss += (v0[0] * v0[0] + v0[1] * v0[1]) + (v0[2] * v0[2] + v0[3] * v0[3]) + (v1[0] * v1[0] + v1[1] * v1[1]) + (v1[2] * v1[2] + v1[3] * v1[3]);
;                     u32x4 w; w.x = cvt_pk_bf16(v0[0], v0[1]); w.y = cvt_pk_bf16(v0[2], v0[3]); w.z = cvt_pk_bf16(v1[0], v1[1]); w.w = cvt_pk_bf16(v1[2], v1[3]);
;                     *(u32x4*)(HB + off) = w;
;                     u32x2e q; q.x = q8x4(v0, gv[bj][0], (float)HQS); q.y = q8x4(v1, gv[bj][1], (float)HQS);
;                     *(u32x2e*)(Q8 + r * LDQ8 + col0 + bj * HALF) = q; }
;                 ss += __shfl_xor(ss, 16); ss += __shfl_xor(ss, 32);
;                 if (fq == 0) SSQP[r * 64 + u.pn * 4 + wc] = ss; }
	v_pk_fma_f32 v[130:131], v[130:131], s[26:27], v[248:249] op_sel_hi:[1,0,1]
	v_mul_f32_e32 v150, v147, v147
	v_mul_f32_e32 v151, v149, v149
	v_pk_fma_f32 v[152:153], v[156:157], s[26:27], v[250:251] op_sel_hi:[1,0,1]
	v_mul_f32_e32 v156, v131, v131
	v_cvt_pk_bf16_f32 v134, v146, v147
	v_cvt_pk_bf16_f32 v135, v148, v149
	v_cvt_pk_bf16_f32 v136, v130, v131
	v_mul_f32_e32 v131, v51, v131
	v_fmac_f32_e32 v150, v146, v146
	v_fmac_f32_e32 v151, v148, v148
	v_mul_f32_e32 v157, v153, v153
	v_mul_f32_e32 v160, v64, v148
	v_fmac_f32_e32 v156, v130, v130
	v_mul_f32_e32 v131, 0x41c00000, v131
	v_add_f32_e32 v148, v150, v151
	v_mul_f32_e32 v149, v65, v149
	v_fmac_f32_e32 v157, v152, v152
	v_med3_f32 v131, v131, s51, v177
	v_add_f32_e32 v148, v148, v156
	v_cvt_pk_bf16_f32 v137, v152, v153
	global_store_dwordx4 v[154:155], v[134:137], off
	v_mul_f32_e32 v159, v62, v146
	v_mul_f32_e32 v147, v63, v147
	v_mul_f32_e32 v136, 0x41c00000, v149
	v_add_f32_e32 v149, 0x4b400000, v131
	v_add_f32_e32 v131, v157, v148
	v_add_f32_e32 v131, v158, v131
	ds_bpermute_b32 v148, v132, v131
	v_mul_f32_e32 v161, v50, v130
	v_mul_f32_e32 v130, 0x41c00000, v159
	v_mul_f32_e32 v134, 0x41c00000, v147
	v_mul_f32_e32 v135, 0x41c00000, v160
	v_med3_f32 v130, v130, s51, v177
	v_med3_f32 v134, v134, s51, v177
	v_med3_f32 v135, v135, s51, v177
	v_med3_f32 v136, v136, s51, v177
	v_add_f32_e32 v130, 0x4b400000, v130
	v_add_f32_e32 v134, 0x4b400000, v134
	v_add_f32_e32 v135, 0x4b400000, v135
	v_add_f32_e32 v136, 0x4b400000, v136
	v_cndmask_b32_e32 v133, v176, v182, vcc
	v_perm_b32 v130, v134, v130, s56
	v_perm_b32 v134, v136, v135, s57
	v_mul_f32_e32 v178, v52, v152
	v_mul_f32_e32 v153, v53, v153
	v_or_b32_e32 v134, v130, v134
	s_waitcnt lgkmcnt(0)
	v_add_f32_e32 v130, v131, v148
	v_lshlrev_b32_e32 v133, 2, v133
	v_mul_f32_e32 v137, 0x41c00000, v161
	v_mul_f32_e32 v146, 0x41c00000, v178
	v_mul_f32_e32 v147, 0x41c00000, v153
	ds_bpermute_b32 v131, v133, v130
	v_med3_f32 v137, v137, s51, v177
	v_med3_f32 v146, v146, s51, v177
	v_med3_f32 v147, v147, s51, v177
	v_add_f32_e32 v137, 0x4b400000, v137
	v_add_f32_e32 v146, 0x4b400000, v146
	v_add_f32_e32 v147, 0x4b400000, v147
	v_perm_b32 v135, v149, v137, s56
	v_perm_b32 v136, v147, v146, s57
	v_or_b32_e32 v135, v135, v136
	global_store_dwordx2 v[144:145], v[134:135], off offset:128
	s_and_saveexec_b64 s[28:29], s[0:1]
	s_cbranch_execz .LBB0_619
	v_lshlrev_b64 v[134:135], 8, v[140:141]
	v_lshl_add_u64 v[134:135], s[22:23], 0, v[134:135]
	s_waitcnt lgkmcnt(0)
	v_add_f32_e32 v130, v130, v131
	global_store_dword v[134:135], v130, off
.LBB0_619:
	s_or_b64 exec, exec, s[28:29]
	s_add_u32 s98, s8, 0x80000
	s_addc_u32 s99, s9, 0
	global_load_dwordx4 v[228:231], v252, s[98:99] nt
	global_load_dwordx4 v[232:235], v252, s[98:99] offset:16 nt
	global_load_dwordx4 v[236:239], v252, s[98:99] offset:512 nt
	global_load_dwordx4 v[240:243], v252, s[98:99] offset:528 nt
	v_or_b32_e32 v130, 16, v140
	s_waitcnt lgkmcnt(0)
	v_ashrrev_i32_e32 v131, 31, v130
	v_lshlrev_b64 v[134:135], 12, v[130:131]
	v_lshl_add_u64 v[148:149], v[134:135], 0, v[138:139]
	v_lshl_add_u64 v[150:151], v[148:149], 2, s[8:9]
	s_nop 0
	s_nop 0
	v_cvt_f32_i32_e32 v127, v127
	v_cvt_f32_i32_e32 v126, v126
	v_cvt_f32_i32_e32 v129, v129
	v_cvt_f32_i32_e32 v128, v128
	v_cvt_f32_i32_e32 v153, v123
	v_cvt_f32_i32_e32 v152, v122
	v_cvt_f32_i32_e32 v125, v125
	v_cvt_f32_i32_e32 v124, v124
	v_lshlrev_b64 v[148:149], 1, v[148:149]
	v_lshl_add_u64 v[154:155], s[14:15], 0, v[148:149]
	v_mad_i64_i32 v[122:123], s[28:29], v130, s50, v[142:143]
	v_cvt_f32_i32_e32 v119, v119
	v_cvt_f32_i32_e32 v118, v118
	v_cvt_f32_i32_e32 v121, v121
	v_cvt_f32_i32_e32 v120, v120
	v_cvt_f32_i32_e32 v115, v115
	v_cvt_f32_i32_e32 v114, v114
	v_cvt_f32_i32_e32 v117, v117
	v_cvt_f32_i32_e32 v116, v116
	v_or_b32_e32 v148, 0x100, v148
	v_lshl_add_u64 v[148:149], s[14:15], 0, v[148:149]
	s_waitcnt vmcnt(8)
	v_pk_fma_f32 v[128:129], v[128:129], s[26:27], v[214:215] op_sel_hi:[1,0,1]
	v_pk_fma_f32 v[156:157], v[126:127], s[26:27], v[212:213] op_sel_hi:[1,0,1]
	s_waitcnt vmcnt(8)
	v_pk_fma_f32 v[146:147], v[124:125], s[26:27], v[218:219] op_sel_hi:[1,0,1]
	v_pk_fma_f32 v[144:145], v[152:153], s[26:27], v[216:217] op_sel_hi:[1,0,1]
	v_cvt_pk_bf16_f32 v124, v156, v157
	v_cvt_pk_bf16_f32 v125, v128, v129
	v_mul_f32_e32 v134, v74, v156
	v_cvt_pk_bf16_f32 v126, v144, v145
	v_cvt_pk_bf16_f32 v127, v146, v147
	v_mul_f32_e32 v135, v75, v157
	v_mul_f32_e32 v136, v76, v128
	v_mul_f32_e32 v137, v77, v129
	v_mul_f32_e32 v141, v66, v144
	v_mul_f32_e32 v152, v67, v145
	v_mul_f32_e32 v153, v68, v146
	v_mul_f32_e32 v158, v69, v147
	global_store_dwordx4 v[154:155], v[124:127], off
	v_mul_f32_e32 v129, v129, v129
	v_fmac_f32_e32 v129, v128, v128
	v_mul_f32_e32 v124, 0x41c00000, v134
	v_mul_f32_e32 v125, 0x41c00000, v135
	v_mul_f32_e32 v126, 0x41c00000, v136
	v_mul_f32_e32 v127, 0x41c00000, v137
	v_mul_f32_e32 v134, 0x41c00000, v141
	v_mul_f32_e32 v135, 0x41c00000, v152
	v_mul_f32_e32 v136, 0x41c00000, v153
	v_mul_f32_e32 v137, 0x41c00000, v158
	v_med3_f32 v124, v124, s51, v177
	v_med3_f32 v125, v125, s51, v177
	v_med3_f32 v126, v126, s51, v177
	v_med3_f32 v127, v127, s51, v177
	v_med3_f32 v134, v134, s51, v177
	v_med3_f32 v135, v135, s51, v177
	v_med3_f32 v136, v136, s51, v177
	v_med3_f32 v137, v137, s51, v177
	v_add_f32_e32 v124, 0x4b400000, v124
	v_add_f32_e32 v125, 0x4b400000, v125
	v_add_f32_e32 v126, 0x4b400000, v126
	v_add_f32_e32 v127, 0x4b400000, v127
	v_add_f32_e32 v134, 0x4b400000, v134
	v_add_f32_e32 v135, 0x4b400000, v135
	v_add_f32_e32 v136, 0x4b400000, v136
	v_add_f32_e32 v137, 0x4b400000, v137
	v_perm_b32 v124, v125, v124, s56
	v_perm_b32 v125, v127, v126, s57
	v_perm_b32 v126, v135, v134, s56
	v_perm_b32 v127, v137, v136, s57
	v_or_b32_e32 v124, v124, v125
	v_or_b32_e32 v125, v126, v127
	global_store_dwordx2 v[122:123], v[124:125], off
	s_nop 0
	s_nop 0
	s_nop 0
	v_mul_f32_e32 v141, v157, v157
	v_fmac_f32_e32 v141, v156, v156
	v_add_f32_e32 v128, v141, v129
	v_mul_f32_e32 v145, v145, v145
	v_mul_f32_e32 v147, v147, v147
	v_fmac_f32_e32 v145, v144, v144
	v_fmac_f32_e32 v147, v146, v146
	v_add_f32_e32 v128, v128, v145
	v_add_f32_e32 v128, v147, v128
	s_waitcnt vmcnt(11)
; __device__ __forceinline__ unsigned cvt_pk_bf16(float lo, float hi) { unsigned r; asm volatile("v_cvt_pk_bf16_f32 %0, %1, %2" : "=v"(r) : "v"(lo), "v"(hi)); return r; }
;     __device__ __forceinline__ void operator()(const f32x4 (&acc)[2][2][4][2], const Unit& u, int wr, int wc, int fr, int fq) const {
;     ...
;             for (int m = 0; m < 4; ++m) { const size_t r = (size_t)(row0 + ai * HALF + m * 16); float ss = 0.f;
; #pragma unroll
;                 for (int bj = 0; bj < 2; ++bj) { const size_t off = r * 4096 + col0 + bj * HALF;
;                     const f32x4 v0 = acc[ai][bj][m][0] * scale + *(const f32x4*)(R + off), v1 = acc[ai][bj][m][1] * scale + *(const f32x4*)(R + off + 4);
;                     ss += (v0[0] * v0[0] + v0[1] * v0[1]) + (v0[2] * v0[2] + v0[3] * v0[3]) + (v1[0] * v1[0] + v1[1] * v1[1]) + (v1[2] * v1[2] + v1[3] * v1[3]);
;                     u32x4 w; w.x = cvt_pk_bf16(v0[0], v0[1]); w.y = cvt_pk_bf16(v0[2], v0[3]); w.z = cvt_pk_bf16(v1[0], v1[1]); w.w = cvt_pk_bf16(v1[2], v1[3]);
;                     *(u32x4*)(HB + off) = w;
;                     u32x2e q; q.x = q8x4(v0, gv[bj][0], (float)HQS); q.y = q8x4(v1, gv[bj][1], (float)HQS);
;                     *(u32x2e*)(Q8 + r * LDQ8 + col0 + bj * HALF) = q; }
;                 ss += __shfl_xor(ss, 16); ss += __shfl_xor(ss, 32);
;                 if (fq == 0) SSQP[r * 64 + u.pn * 4 + wc] = ss; }
	v_pk_fma_f32 v[120:121], v[120:121], s[26:27], v[222:223] op_sel_hi:[1,0,1]
	v_pk_fma_f32 v[118:119], v[118:119], s[26:27], v[220:221] op_sel_hi:[1,0,1]
	s_waitcnt vmcnt(11)
	v_pk_fma_f32 v[126:127], v[114:115], s[26:27], v[224:225] op_sel_hi:[1,0,1]
	v_mul_f32_e32 v129, v119, v119
	v_mul_f32_e32 v134, v121, v121
	v_pk_fma_f32 v[124:125], v[116:117], s[26:27], v[226:227] op_sel_hi:[1,0,1]
	v_mul_f32_e32 v135, v127, v127
	v_cvt_pk_bf16_f32 v114, v118, v119
	v_cvt_pk_bf16_f32 v115, v120, v121
	v_cvt_pk_bf16_f32 v116, v126, v127
	v_cvt_pk_bf16_f32 v117, v124, v125
	v_mul_f32_e32 v137, v62, v118
	v_mul_f32_e32 v119, v63, v119
	v_mul_f32_e32 v141, v64, v120
	v_mul_f32_e32 v121, v65, v121
	v_fmac_f32_e32 v129, v118, v118
	v_fmac_f32_e32 v134, v120, v120
	v_mul_f32_e32 v136, v125, v125
	v_fmac_f32_e32 v135, v126, v126
	global_store_dwordx4 v[148:149], v[114:117], off
	v_fmac_f32_e32 v136, v124, v124
	v_mul_f32_e32 v144, v50, v126
	v_mul_f32_e32 v114, 0x41c00000, v137
	v_mul_f32_e32 v115, 0x41c00000, v119
	v_mul_f32_e32 v116, 0x41c00000, v141
	v_mul_f32_e32 v117, 0x41c00000, v121
	v_add_f32_e32 v121, v129, v134
	v_med3_f32 v114, v114, s51, v177
	v_med3_f32 v115, v115, s51, v177
	v_med3_f32 v116, v116, s51, v177
	v_med3_f32 v117, v117, s51, v177
	v_add_f32_e32 v121, v121, v135
	v_add_f32_e32 v114, 0x4b400000, v114
	v_add_f32_e32 v115, 0x4b400000, v115
	v_add_f32_e32 v116, 0x4b400000, v116
	v_add_f32_e32 v117, 0x4b400000, v117
	v_add_f32_e32 v121, v136, v121
	v_perm_b32 v114, v115, v114, s56
	v_perm_b32 v115, v117, v116, s57
	v_add_f32_e32 v117, v128, v121
	v_or_b32_e32 v116, v114, v115
	ds_bpermute_b32 v114, v132, v117
	v_mul_f32_e32 v115, v53, v125
	v_mul_f32_e32 v115, 0x41c00000, v115
	v_mul_f32_e32 v127, v51, v127
	v_mul_f32_e32 v145, v52, v124
	v_med3_f32 v115, v115, s51, v177
	s_waitcnt lgkmcnt(0)
	v_add_f32_e32 v114, v117, v114
	v_mul_f32_e32 v118, 0x41c00000, v144
	v_mul_f32_e32 v119, 0x41c00000, v127
	v_mul_f32_e32 v120, 0x41c00000, v145
	v_add_f32_e32 v121, 0x4b400000, v115
	ds_bpermute_b32 v115, v133, v114
	v_med3_f32 v118, v118, s51, v177
	v_med3_f32 v119, v119, s51, v177
	v_med3_f32 v120, v120, s51, v177
	v_add_f32_e32 v118, 0x4b400000, v118
	v_add_f32_e32 v119, 0x4b400000, v119
	v_add_f32_e32 v120, 0x4b400000, v120
	v_perm_b32 v117, v119, v118, s56
	v_perm_b32 v118, v121, v120, s57
	v_or_b32_e32 v117, v117, v118
	global_store_dwordx2 v[122:123], v[116:117], off offset:128
	s_and_saveexec_b64 s[28:29], s[0:1]
	s_cbranch_execz .LBB0_621
	v_lshlrev_b64 v[116:117], 8, v[130:131]
	v_lshl_add_u64 v[116:117], s[22:23], 0, v[116:117]
	s_waitcnt lgkmcnt(0)
	v_add_f32_e32 v114, v114, v115
	global_store_dword v[116:117], v114, off
.LBB0_621:
	s_or_b64 exec, exec, s[28:29]
	s_add_u32 s98, s8, 0xc0000
	s_addc_u32 s99, s9, 0
	global_load_dwordx4 v[212:215], v252, s[98:99] nt
	global_load_dwordx4 v[216:219], v252, s[98:99] offset:16 nt
	global_load_dwordx4 v[220:223], v252, s[98:99] offset:512 nt
	global_load_dwordx4 v[224:227], v252, s[98:99] offset:528 nt
	v_or_b32_e32 v114, 32, v140
	s_waitcnt lgkmcnt(0)
	v_ashrrev_i32_e32 v115, 31, v114
	v_lshlrev_b64 v[116:117], 12, v[114:115]
	v_lshl_add_u64 v[124:125], v[116:117], 0, v[138:139]
	v_lshl_add_u64 v[126:127], v[124:125], 2, s[8:9]
	s_nop 0
	s_nop 0
	v_cvt_f32_i32_e32 v111, v111
	v_cvt_f32_i32_e32 v110, v110
	v_cvt_f32_i32_e32 v113, v113
	v_cvt_f32_i32_e32 v112, v112
	v_cvt_f32_i32_e32 v129, v107
	v_cvt_f32_i32_e32 v128, v106
	v_cvt_f32_i32_e32 v109, v109
	v_cvt_f32_i32_e32 v108, v108
	v_lshlrev_b64 v[124:125], 1, v[124:125]
	v_lshl_add_u64 v[130:131], s[14:15], 0, v[124:125]
	v_mad_i64_i32 v[106:107], s[28:29], v114, s50, v[142:143]
	v_cvt_f32_i32_e32 v103, v103
	v_cvt_f32_i32_e32 v102, v102
	v_cvt_f32_i32_e32 v105, v105
	v_cvt_f32_i32_e32 v104, v104
	v_cvt_f32_i32_e32 v99, v99
	v_cvt_f32_i32_e32 v98, v98
	v_cvt_f32_i32_e32 v101, v101
	v_cvt_f32_i32_e32 v100, v100
	v_or_b32_e32 v124, 0x100, v124
	v_lshl_add_u64 v[124:125], s[14:15], 0, v[124:125]
	s_waitcnt vmcnt(8)
	v_pk_fma_f32 v[112:113], v[112:113], s[26:27], v[230:231] op_sel_hi:[1,0,1]
	v_pk_fma_f32 v[134:135], v[110:111], s[26:27], v[228:229] op_sel_hi:[1,0,1]
	s_waitcnt vmcnt(8)
	v_pk_fma_f32 v[122:123], v[108:109], s[26:27], v[234:235] op_sel_hi:[1,0,1]
	v_pk_fma_f32 v[120:121], v[128:129], s[26:27], v[232:233] op_sel_hi:[1,0,1]
	v_cvt_pk_bf16_f32 v108, v134, v135
	v_cvt_pk_bf16_f32 v109, v112, v113
	v_mul_f32_e32 v116, v74, v134
	v_cvt_pk_bf16_f32 v110, v120, v121
	v_cvt_pk_bf16_f32 v111, v122, v123
	v_mul_f32_e32 v117, v75, v135
	v_mul_f32_e32 v118, v76, v112
	v_mul_f32_e32 v119, v77, v113
	v_mul_f32_e32 v128, v66, v120
	v_mul_f32_e32 v129, v67, v121
	v_mul_f32_e32 v136, v68, v122
	v_mul_f32_e32 v137, v69, v123
	global_store_dwordx4 v[130:131], v[108:111], off
	v_mul_f32_e32 v113, v113, v113
	v_fmac_f32_e32 v113, v112, v112
	v_mul_f32_e32 v108, 0x41c00000, v116
	v_mul_f32_e32 v109, 0x41c00000, v117
	v_mul_f32_e32 v110, 0x41c00000, v118
	v_mul_f32_e32 v111, 0x41c00000, v119
	v_mul_f32_e32 v116, 0x41c00000, v128
	v_mul_f32_e32 v117, 0x41c00000, v129
	v_mul_f32_e32 v118, 0x41c00000, v136
	v_mul_f32_e32 v119, 0x41c00000, v137
	v_med3_f32 v108, v108, s51, v177
	v_med3_f32 v109, v109, s51, v177
	v_med3_f32 v110, v110, s51, v177
	v_med3_f32 v111, v111, s51, v177
	v_med3_f32 v116, v116, s51, v177
	v_med3_f32 v117, v117, s51, v177
	v_med3_f32 v118, v118, s51, v177
	v_med3_f32 v119, v119, s51, v177
	v_add_f32_e32 v108, 0x4b400000, v108
	v_add_f32_e32 v109, 0x4b400000, v109
	v_add_f32_e32 v110, 0x4b400000, v110
	v_add_f32_e32 v111, 0x4b400000, v111
	v_add_f32_e32 v116, 0x4b400000, v116
	v_add_f32_e32 v117, 0x4b400000, v117
	v_add_f32_e32 v118, 0x4b400000, v118
	v_add_f32_e32 v119, 0x4b400000, v119
	v_perm_b32 v108, v109, v108, s56
	v_perm_b32 v109, v111, v110, s57
	v_perm_b32 v110, v117, v116, s56
	v_perm_b32 v111, v119, v118, s57
	v_or_b32_e32 v108, v108, v109
	v_or_b32_e32 v109, v110, v111
	global_store_dwordx2 v[106:107], v[108:109], off
	s_nop 0
	s_nop 0
	s_nop 0
	v_mul_f32_e32 v126, v135, v135
	v_fmac_f32_e32 v126, v134, v134
	v_mul_f32_e32 v121, v121, v121
	v_add_f32_e32 v112, v126, v113
	v_fmac_f32_e32 v121, v120, v120
	v_mul_f32_e32 v123, v123, v123
	v_fmac_f32_e32 v123, v122, v122
	v_add_f32_e32 v112, v112, v121
	v_add_f32_e32 v112, v123, v112
	s_waitcnt vmcnt(11)
; __device__ __forceinline__ unsigned cvt_pk_bf16(float lo, float hi) { unsigned r; asm volatile("v_cvt_pk_bf16_f32 %0, %1, %2" : "=v"(r) : "v"(lo), "v"(hi)); return r; }
;     __device__ __forceinline__ void operator()(const f32x4 (&acc)[2][2][4][2], const Unit& u, int wr, int wc, int fr, int fq) const {
;     ...
;             for (int m = 0; m < 4; ++m) { const size_t r = (size_t)(row0 + ai * HALF + m * 16); float ss = 0.f;
; #pragma unroll
;                 for (int bj = 0; bj < 2; ++bj) { const size_t off = r * 4096 + col0 + bj * HALF;
;                     const f32x4 v0 = acc[ai][bj][m][0] * scale + *(const f32x4*)(R + off), v1 = acc[ai][bj][m][1] * scale + *(const f32x4*)(R + off + 4);
;                     ss += (v0[0] * v0[0] + v0[1] * v0[1]) + (v0[2] * v0[2] + v0[3] * v0[3]) + (v1[0] * v1[0] + v1[1] * v1[1]) + (v1[2] * v1[2] + v1[3] * v1[3]);
;                     u32x4 w; w.x = cvt_pk_bf16(v0[0], v0[1]); w.y = cvt_pk_bf16(v0[2], v0[3]); w.z = cvt_pk_bf16(v1[0], v1[1]); w.w = cvt_pk_bf16(v1[2], v1[3]);
;                     *(u32x4*)(HB + off) = w;
;                     u32x2e q; q.x = q8x4(v0, gv[bj][0], (float)HQS); q.y = q8x4(v1, gv[bj][1], (float)HQS);
;                     *(u32x2e*)(Q8 + r * LDQ8 + col0 + bj * HALF) = q; }
;                 ss += __shfl_xor(ss, 16); ss += __shfl_xor(ss, 32);
;                 if (fq == 0) SSQP[r * 64 + u.pn * 4 + wc] = ss; }
	v_pk_fma_f32 v[104:105], v[104:105], s[26:27], v[238:239] op_sel_hi:[1,0,1]
	v_pk_fma_f32 v[102:103], v[102:103], s[26:27], v[236:237] op_sel_hi:[1,0,1]
	s_waitcnt vmcnt(11)
	v_pk_fma_f32 v[110:111], v[98:99], s[26:27], v[240:241] op_sel_hi:[1,0,1]
	v_mul_f32_e32 v113, v103, v103
	v_mul_f32_e32 v116, v105, v105
	v_pk_fma_f32 v[108:109], v[100:101], s[26:27], v[242:243] op_sel_hi:[1,0,1]
	v_mul_f32_e32 v117, v111, v111
	v_cvt_pk_bf16_f32 v98, v102, v103
	v_cvt_pk_bf16_f32 v99, v104, v105
	v_cvt_pk_bf16_f32 v100, v110, v111
	v_cvt_pk_bf16_f32 v101, v108, v109
	v_mul_f32_e32 v119, v62, v102
	v_mul_f32_e32 v103, v63, v103
	v_mul_f32_e32 v120, v64, v104
	v_mul_f32_e32 v105, v65, v105
	v_fmac_f32_e32 v113, v102, v102
	v_fmac_f32_e32 v116, v104, v104
	v_mul_f32_e32 v118, v109, v109
	v_fmac_f32_e32 v117, v110, v110
	global_store_dwordx4 v[124:125], v[98:101], off
	v_fmac_f32_e32 v118, v108, v108
	v_mul_f32_e32 v121, v50, v110
	v_mul_f32_e32 v98, 0x41c00000, v119
	v_mul_f32_e32 v99, 0x41c00000, v103
	v_mul_f32_e32 v100, 0x41c00000, v120
	v_mul_f32_e32 v101, 0x41c00000, v105
	v_add_f32_e32 v105, v113, v116
	v_med3_f32 v98, v98, s51, v177
	v_med3_f32 v99, v99, s51, v177
	v_med3_f32 v100, v100, s51, v177
	v_med3_f32 v101, v101, s51, v177
	v_add_f32_e32 v105, v105, v117
	v_add_f32_e32 v98, 0x4b400000, v98
	v_add_f32_e32 v99, 0x4b400000, v99
	v_add_f32_e32 v100, 0x4b400000, v100
	v_add_f32_e32 v101, 0x4b400000, v101
	v_add_f32_e32 v105, v118, v105
	v_perm_b32 v98, v99, v98, s56
	v_perm_b32 v99, v101, v100, s57
	v_add_f32_e32 v101, v112, v105
	v_or_b32_e32 v100, v98, v99
	ds_bpermute_b32 v98, v132, v101
	v_mul_f32_e32 v99, v53, v109
	v_mul_f32_e32 v99, 0x41c00000, v99
	v_mul_f32_e32 v111, v51, v111
	v_mul_f32_e32 v122, v52, v108
	v_med3_f32 v99, v99, s51, v177
	s_waitcnt lgkmcnt(0)
	v_add_f32_e32 v98, v101, v98
	v_mul_f32_e32 v102, 0x41c00000, v121
	v_mul_f32_e32 v103, 0x41c00000, v111
	v_mul_f32_e32 v104, 0x41c00000, v122
	v_add_f32_e32 v105, 0x4b400000, v99
	ds_bpermute_b32 v99, v133, v98
	v_med3_f32 v102, v102, s51, v177
	v_med3_f32 v103, v103, s51, v177
	v_med3_f32 v104, v104, s51, v177
	v_add_f32_e32 v102, 0x4b400000, v102
	v_add_f32_e32 v103, 0x4b400000, v103
	v_add_f32_e32 v104, 0x4b400000, v104
	v_perm_b32 v101, v103, v102, s56
	v_perm_b32 v102, v105, v104, s57
	v_or_b32_e32 v101, v101, v102
	global_store_dwordx2 v[106:107], v[100:101], off offset:128
	s_and_saveexec_b64 s[28:29], s[0:1]
	s_cbranch_execz .LBB0_623
	v_lshlrev_b64 v[100:101], 8, v[114:115]
	v_lshl_add_u64 v[100:101], s[22:23], 0, v[100:101]
	s_waitcnt lgkmcnt(0)
	v_add_f32_e32 v98, v98, v99
	global_store_dword v[100:101], v98, off
.LBB0_623:
	s_or_b64 exec, exec, s[28:29]
	s_add_u32 s98, s8, 0x200000
	s_addc_u32 s99, s9, 0
	global_load_dwordx4 v[228:231], v252, s[98:99] nt
	global_load_dwordx4 v[232:235], v252, s[98:99] offset:16 nt
	global_load_dwordx4 v[236:239], v252, s[98:99] offset:512 nt
	global_load_dwordx4 v[240:243], v252, s[98:99] offset:528 nt
	v_or_b32_e32 v98, 48, v140
	s_waitcnt lgkmcnt(0)
	v_ashrrev_i32_e32 v99, 31, v98
	v_lshlrev_b64 v[100:101], 12, v[98:99]
	v_lshl_add_u64 v[108:109], v[100:101], 0, v[138:139]
	v_lshl_add_u64 v[110:111], v[108:109], 2, s[8:9]
	s_nop 0
	s_nop 0
	v_cvt_f32_i32_e32 v95, v95
	v_cvt_f32_i32_e32 v94, v94
	v_cvt_f32_i32_e32 v97, v97
	v_cvt_f32_i32_e32 v96, v96
	v_cvt_f32_i32_e32 v113, v91
	v_cvt_f32_i32_e32 v112, v90
	v_cvt_f32_i32_e32 v93, v93
	v_cvt_f32_i32_e32 v92, v92
	v_lshlrev_b64 v[108:109], 1, v[108:109]
	v_lshl_add_u64 v[114:115], s[14:15], 0, v[108:109]
	v_mad_i64_i32 v[90:91], s[28:29], v98, s50, v[142:143]
	v_cvt_f32_i32_e32 v87, v87
	v_cvt_f32_i32_e32 v86, v86
	v_cvt_f32_i32_e32 v89, v89
	v_cvt_f32_i32_e32 v88, v88
	v_cvt_f32_i32_e32 v83, v83
	v_cvt_f32_i32_e32 v82, v82
	v_cvt_f32_i32_e32 v85, v85
	v_cvt_f32_i32_e32 v84, v84
	v_or_b32_e32 v108, 0x100, v108
	v_lshl_add_u64 v[108:109], s[14:15], 0, v[108:109]
	s_waitcnt vmcnt(8)
	v_pk_fma_f32 v[96:97], v[96:97], s[26:27], v[214:215] op_sel_hi:[1,0,1]
	v_pk_fma_f32 v[116:117], v[94:95], s[26:27], v[212:213] op_sel_hi:[1,0,1]
	s_waitcnt vmcnt(8)
	v_pk_fma_f32 v[106:107], v[92:93], s[26:27], v[218:219] op_sel_hi:[1,0,1]
	v_pk_fma_f32 v[104:105], v[112:113], s[26:27], v[216:217] op_sel_hi:[1,0,1]
	v_cvt_pk_bf16_f32 v92, v116, v117
	v_cvt_pk_bf16_f32 v93, v96, v97
	v_mul_f32_e32 v100, v74, v116
	v_cvt_pk_bf16_f32 v94, v104, v105
	v_cvt_pk_bf16_f32 v95, v106, v107
	v_mul_f32_e32 v101, v75, v117
	v_mul_f32_e32 v102, v76, v96
	v_mul_f32_e32 v103, v77, v97
	v_mul_f32_e32 v112, v66, v104
	v_mul_f32_e32 v113, v67, v105
	v_mul_f32_e32 v118, v68, v106
	v_mul_f32_e32 v119, v69, v107
	global_store_dwordx4 v[114:115], v[92:95], off
	v_mul_f32_e32 v97, v97, v97
	v_fmac_f32_e32 v97, v96, v96
	v_mul_f32_e32 v92, 0x41c00000, v100
	v_mul_f32_e32 v93, 0x41c00000, v101
	v_mul_f32_e32 v94, 0x41c00000, v102
	v_mul_f32_e32 v95, 0x41c00000, v103
	v_mul_f32_e32 v100, 0x41c00000, v112
	v_mul_f32_e32 v101, 0x41c00000, v113
	v_mul_f32_e32 v102, 0x41c00000, v118
	v_mul_f32_e32 v103, 0x41c00000, v119
	v_med3_f32 v92, v92, s51, v177
	v_med3_f32 v93, v93, s51, v177
	v_med3_f32 v94, v94, s51, v177
	v_med3_f32 v95, v95, s51, v177
	v_med3_f32 v100, v100, s51, v177
	v_med3_f32 v101, v101, s51, v177
	v_med3_f32 v102, v102, s51, v177
	v_med3_f32 v103, v103, s51, v177
	v_add_f32_e32 v92, 0x4b400000, v92
	v_add_f32_e32 v93, 0x4b400000, v93
	v_add_f32_e32 v94, 0x4b400000, v94
	v_add_f32_e32 v95, 0x4b400000, v95
	v_add_f32_e32 v100, 0x4b400000, v100
	v_add_f32_e32 v101, 0x4b400000, v101
	v_add_f32_e32 v102, 0x4b400000, v102
	v_add_f32_e32 v103, 0x4b400000, v103
	v_perm_b32 v92, v93, v92, s56
	v_perm_b32 v93, v95, v94, s57
	v_perm_b32 v94, v101, v100, s56
	v_perm_b32 v95, v103, v102, s57
	v_or_b32_e32 v92, v92, v93
	v_or_b32_e32 v93, v94, v95
	global_store_dwordx2 v[90:91], v[92:93], off
	s_nop 0
	s_nop 0
	s_nop 0
	v_mul_f32_e32 v110, v117, v117
	v_fmac_f32_e32 v110, v116, v116
	v_mul_f32_e32 v105, v105, v105
	v_add_f32_e32 v96, v110, v97
	v_fmac_f32_e32 v105, v104, v104
	v_mul_f32_e32 v107, v107, v107
	v_fmac_f32_e32 v107, v106, v106
	v_add_f32_e32 v96, v96, v105
	v_add_f32_e32 v96, v107, v96
	s_waitcnt vmcnt(11)
; __device__ __forceinline__ unsigned cvt_pk_bf16(float lo, float hi) { unsigned r; asm volatile("v_cvt_pk_bf16_f32 %0, %1, %2" : "=v"(r) : "v"(lo), "v"(hi)); return r; }
;     __device__ __forceinline__ void operator()(const f32x4 (&acc)[2][2][4][2], const Unit& u, int wr, int wc, int fr, int fq) const {
;     ...
;             for (int m = 0; m < 4; ++m) { const size_t r = (size_t)(row0 + ai * HALF + m * 16); float ss = 0.f;
; #pragma unroll
;                 for (int bj = 0; bj < 2; ++bj) { const size_t off = r * 4096 + col0 + bj * HALF;
;                     const f32x4 v0 = acc[ai][bj][m][0] * scale + *(const f32x4*)(R + off), v1 = acc[ai][bj][m][1] * scale + *(const f32x4*)(R + off + 4);
;                     ss += (v0[0] * v0[0] + v0[1] * v0[1]) + (v0[2] * v0[2] + v0[3] * v0[3]) + (v1[0] * v1[0] + v1[1] * v1[1]) + (v1[2] * v1[2] + v1[3] * v1[3]);
;                     u32x4 w; w.x = cvt_pk_bf16(v0[0], v0[1]); w.y = cvt_pk_bf16(v0[2], v0[3]); w.z = cvt_pk_bf16(v1[0], v1[1]); w.w = cvt_pk_bf16(v1[2], v1[3]);
;                     *(u32x4*)(HB + off) = w;
;                     u32x2e q; q.x = q8x4(v0, gv[bj][0], (float)HQS); q.y = q8x4(v1, gv[bj][1], (float)HQS);
;                     *(u32x2e*)(Q8 + r * LDQ8 + col0 + bj * HALF) = q; }
;                 ss += __shfl_xor(ss, 16); ss += __shfl_xor(ss, 32);
;                 if (fq == 0) SSQP[r * 64 + u.pn * 4 + wc] = ss; }
	v_pk_fma_f32 v[88:89], v[88:89], s[26:27], v[222:223] op_sel_hi:[1,0,1]
	v_pk_fma_f32 v[86:87], v[86:87], s[26:27], v[220:221] op_sel_hi:[1,0,1]
	s_waitcnt vmcnt(11)
	v_pk_fma_f32 v[94:95], v[82:83], s[26:27], v[224:225] op_sel_hi:[1,0,1]
	v_mul_f32_e32 v97, v87, v87
	v_mul_f32_e32 v100, v89, v89
	v_pk_fma_f32 v[92:93], v[84:85], s[26:27], v[226:227] op_sel_hi:[1,0,1]
	v_mul_f32_e32 v101, v95, v95
	v_cvt_pk_bf16_f32 v82, v86, v87
	v_cvt_pk_bf16_f32 v83, v88, v89
	v_cvt_pk_bf16_f32 v84, v94, v95
	v_cvt_pk_bf16_f32 v85, v92, v93
	v_mul_f32_e32 v103, v62, v86
	v_mul_f32_e32 v87, v63, v87
	v_mul_f32_e32 v104, v64, v88
	v_mul_f32_e32 v89, v65, v89
	v_fmac_f32_e32 v97, v86, v86
	v_fmac_f32_e32 v100, v88, v88
	v_mul_f32_e32 v102, v93, v93
	v_fmac_f32_e32 v101, v94, v94
	global_store_dwordx4 v[108:109], v[82:85], off
	v_fmac_f32_e32 v102, v92, v92
	v_mul_f32_e32 v105, v50, v94
	v_mul_f32_e32 v82, 0x41c00000, v103
	v_mul_f32_e32 v83, 0x41c00000, v87
	v_mul_f32_e32 v84, 0x41c00000, v104
	v_mul_f32_e32 v85, 0x41c00000, v89
	v_add_f32_e32 v89, v97, v100
	v_med3_f32 v82, v82, s51, v177
	v_med3_f32 v83, v83, s51, v177
	v_med3_f32 v84, v84, s51, v177
	v_med3_f32 v85, v85, s51, v177
	v_add_f32_e32 v89, v89, v101
	v_add_f32_e32 v82, 0x4b400000, v82
	v_add_f32_e32 v83, 0x4b400000, v83
	v_add_f32_e32 v84, 0x4b400000, v84
	v_add_f32_e32 v85, 0x4b400000, v85
	v_add_f32_e32 v89, v102, v89
	v_perm_b32 v82, v83, v82, s56
	v_perm_b32 v83, v85, v84, s57
	v_add_f32_e32 v85, v96, v89
	v_or_b32_e32 v84, v82, v83
	ds_bpermute_b32 v82, v132, v85
	v_mul_f32_e32 v83, v53, v93
	v_mul_f32_e32 v83, 0x41c00000, v83
	v_mul_f32_e32 v95, v51, v95
	v_mul_f32_e32 v106, v52, v92
	v_med3_f32 v83, v83, s51, v177
	s_waitcnt lgkmcnt(0)
	v_add_f32_e32 v82, v85, v82
	v_mul_f32_e32 v86, 0x41c00000, v105
	v_mul_f32_e32 v87, 0x41c00000, v95
	v_mul_f32_e32 v88, 0x41c00000, v106
	v_add_f32_e32 v89, 0x4b400000, v83
	ds_bpermute_b32 v83, v133, v82
	v_med3_f32 v86, v86, s51, v177
	v_med3_f32 v87, v87, s51, v177
	v_med3_f32 v88, v88, s51, v177
	v_add_f32_e32 v86, 0x4b400000, v86
	v_add_f32_e32 v87, 0x4b400000, v87
	v_add_f32_e32 v88, 0x4b400000, v88
	v_perm_b32 v85, v87, v86, s56
	v_perm_b32 v86, v89, v88, s57
	v_or_b32_e32 v85, v85, v86
	global_store_dwordx2 v[90:91], v[84:85], off offset:128
	s_and_saveexec_b64 s[28:29], s[0:1]
	s_cbranch_execz .LBB0_625
	v_lshlrev_b64 v[84:85], 8, v[98:99]
	v_lshl_add_u64 v[84:85], s[22:23], 0, v[84:85]
	s_waitcnt lgkmcnt(0)
	v_add_f32_e32 v82, v82, v83
	global_store_dword v[84:85], v82, off
.LBB0_625:
	s_or_b64 exec, exec, s[28:29]
	s_add_u32 s98, s8, 0x240000
	s_addc_u32 s99, s9, 0
	global_load_dwordx4 v[212:215], v252, s[98:99] nt
	global_load_dwordx4 v[216:219], v252, s[98:99] offset:16 nt
	global_load_dwordx4 v[220:223], v252, s[98:99] offset:512 nt
	global_load_dwordx4 v[224:227], v252, s[98:99] offset:528 nt
	v_add_u32_e32 v82, 0x80, v140
	s_waitcnt lgkmcnt(0)
	v_ashrrev_i32_e32 v83, 31, v82
	v_lshlrev_b64 v[84:85], 12, v[82:83]
	v_lshl_add_u64 v[92:93], v[84:85], 0, v[138:139]
	v_lshl_add_u64 v[94:95], v[92:93], 2, s[8:9]
	s_nop 0
	s_nop 0
	v_cvt_f32_i32_e32 v79, v79
	v_cvt_f32_i32_e32 v78, v78
	v_cvt_f32_i32_e32 v81, v81
	v_cvt_f32_i32_e32 v80, v80
	v_cvt_f32_i32_e32 v97, v71
	v_cvt_f32_i32_e32 v96, v70
	v_cvt_f32_i32_e32 v73, v73
	v_cvt_f32_i32_e32 v72, v72
	v_lshlrev_b64 v[92:93], 1, v[92:93]
	v_lshl_add_u64 v[98:99], s[14:15], 0, v[92:93]
	v_mad_i64_i32 v[70:71], s[28:29], v82, s50, v[142:143]
	v_cvt_f32_i32_e32 v59, v59
	v_cvt_f32_i32_e32 v58, v58
	v_cvt_f32_i32_e32 v61, v61
	v_cvt_f32_i32_e32 v60, v60
	v_cvt_f32_i32_e32 v55, v55
	v_cvt_f32_i32_e32 v54, v54
	v_or_b32_e32 v92, 0x100, v92
	v_cvt_f32_i32_e32 v57, v57
	v_cvt_f32_i32_e32 v56, v56
	s_waitcnt vmcnt(8)
	v_pk_fma_f32 v[100:101], v[80:81], s[26:27], v[230:231] op_sel_hi:[1,0,1]
	v_pk_fma_f32 v[102:103], v[78:79], s[26:27], v[228:229] op_sel_hi:[1,0,1]
	s_waitcnt vmcnt(8)
	v_pk_fma_f32 v[72:73], v[72:73], s[26:27], v[234:235] op_sel_hi:[1,0,1]
	v_pk_fma_f32 v[88:89], v[96:97], s[26:27], v[232:233] op_sel_hi:[1,0,1]
	v_cvt_pk_bf16_f32 v78, v102, v103
	v_cvt_pk_bf16_f32 v79, v100, v101
	v_mul_f32_e32 v84, v74, v102
	v_cvt_pk_bf16_f32 v80, v88, v89
	v_cvt_pk_bf16_f32 v81, v72, v73
	v_mul_f32_e32 v85, v75, v103
	v_mul_f32_e32 v86, v76, v100
	v_mul_f32_e32 v87, v77, v101
	v_mul_f32_e32 v90, v66, v88
	v_mul_f32_e32 v91, v67, v89
	v_mul_f32_e32 v96, v68, v72
	v_mul_f32_e32 v97, v69, v73
	global_store_dwordx4 v[98:99], v[78:81], off
	v_mul_f32_e32 v89, v89, v89
	v_mul_f32_e32 v73, v73, v73
	v_mul_f32_e32 v78, 0x41c00000, v84
	v_mul_f32_e32 v79, 0x41c00000, v85
	v_mul_f32_e32 v80, 0x41c00000, v86
	v_mul_f32_e32 v81, 0x41c00000, v87
	v_mul_f32_e32 v84, 0x41c00000, v90
	v_mul_f32_e32 v85, 0x41c00000, v91
	v_mul_f32_e32 v86, 0x41c00000, v96
	v_mul_f32_e32 v87, 0x41c00000, v97
	v_med3_f32 v78, v78, s51, v177
	v_med3_f32 v79, v79, s51, v177
	v_med3_f32 v80, v80, s51, v177
	v_med3_f32 v81, v81, s51, v177
	v_med3_f32 v84, v84, s51, v177
	v_med3_f32 v85, v85, s51, v177
	v_med3_f32 v86, v86, s51, v177
	v_med3_f32 v87, v87, s51, v177
	v_add_f32_e32 v78, 0x4b400000, v78
	v_add_f32_e32 v79, 0x4b400000, v79
	v_add_f32_e32 v80, 0x4b400000, v80
	v_add_f32_e32 v81, 0x4b400000, v81
	v_add_f32_e32 v84, 0x4b400000, v84
	v_add_f32_e32 v85, 0x4b400000, v85
	v_add_f32_e32 v86, 0x4b400000, v86
	v_add_f32_e32 v87, 0x4b400000, v87
	v_perm_b32 v78, v79, v78, s56
	v_perm_b32 v79, v81, v80, s57
	v_perm_b32 v80, v85, v84, s56
	v_perm_b32 v81, v87, v86, s57
	v_or_b32_e32 v78, v78, v79
	v_or_b32_e32 v79, v80, v81
	global_store_dwordx2 v[70:71], v[78:79], off
	s_nop 0
	s_nop 0
	s_nop 0
	v_lshl_add_u64 v[90:91], s[14:15], 0, v[92:93]
	v_mul_f32_e32 v92, v103, v103
	v_mul_f32_e32 v93, v101, v101
	v_fmac_f32_e32 v92, v102, v102
	v_fmac_f32_e32 v93, v100, v100
	v_fmac_f32_e32 v89, v88, v88
	v_fmac_f32_e32 v73, v72, v72
	v_add_f32_e32 v72, v92, v93
	v_add_f32_e32 v72, v72, v89
	v_add_f32_e32 v88, v73, v72
	s_waitcnt vmcnt(11)
; __device__ __forceinline__ unsigned cvt_pk_bf16(float lo, float hi) { unsigned r; asm volatile("v_cvt_pk_bf16_f32 %0, %1, %2" : "=v"(r) : "v"(lo), "v"(hi)); return r; }
;     __device__ __forceinline__ void operator()(const f32x4 (&acc)[2][2][4][2], const Unit& u, int wr, int wc, int fr, int fq) const {
;     ...
;             for (int m = 0; m < 4; ++m) { const size_t r = (size_t)(row0 + ai * HALF + m * 16); float ss = 0.f;
; #pragma unroll
;                 for (int bj = 0; bj < 2; ++bj) { const size_t off = r * 4096 + col0 + bj * HALF;
;                     const f32x4 v0 = acc[ai][bj][m][0] * scale + *(const f32x4*)(R + off), v1 = acc[ai][bj][m][1] * scale + *(const f32x4*)(R + off + 4);
;                     ss += (v0[0] * v0[0] + v0[1] * v0[1]) + (v0[2] * v0[2] + v0[3] * v0[3]) + (v1[0] * v1[0] + v1[1] * v1[1]) + (v1[2] * v1[2] + v1[3] * v1[3]);
;                     u32x4 w; w.x = cvt_pk_bf16(v0[0], v0[1]); w.y = cvt_pk_bf16(v0[2], v0[3]); w.z = cvt_pk_bf16(v1[0], v1[1]); w.w = cvt_pk_bf16(v1[2], v1[3]);
;                     *(u32x4*)(HB + off) = w;
;                     u32x2e q; q.x = q8x4(v0, gv[bj][0], (float)HQS); q.y = q8x4(v1, gv[bj][1], (float)HQS);
;                     *(u32x2e*)(Q8 + r * LDQ8 + col0 + bj * HALF) = q; }
;                 ss += __shfl_xor(ss, 16); ss += __shfl_xor(ss, 32);
;                 if (fq == 0) SSQP[r * 64 + u.pn * 4 + wc] = ss; }
	v_pk_fma_f32 v[60:61], v[60:61], s[26:27], v[238:239] op_sel_hi:[1,0,1]
	v_pk_fma_f32 v[58:59], v[58:59], s[26:27], v[236:237] op_sel_hi:[1,0,1]
	s_waitcnt vmcnt(11)
	v_pk_fma_f32 v[78:79], v[54:55], s[26:27], v[240:241] op_sel_hi:[1,0,1]
	v_mul_f32_e32 v80, v59, v59
	v_mul_f32_e32 v81, v61, v61
	v_pk_fma_f32 v[72:73], v[56:57], s[26:27], v[242:243] op_sel_hi:[1,0,1]
	v_mul_f32_e32 v84, v79, v79
	v_cvt_pk_bf16_f32 v54, v58, v59
	v_cvt_pk_bf16_f32 v55, v60, v61
	v_cvt_pk_bf16_f32 v56, v78, v79
	v_cvt_pk_bf16_f32 v57, v72, v73
	v_mul_f32_e32 v86, v62, v58
	v_mul_f32_e32 v59, v63, v59
	v_mul_f32_e32 v87, v64, v60
	v_mul_f32_e32 v61, v65, v61
	v_fmac_f32_e32 v80, v58, v58
	v_fmac_f32_e32 v81, v60, v60
	v_mul_f32_e32 v85, v73, v73
	v_fmac_f32_e32 v84, v78, v78
	global_store_dwordx4 v[90:91], v[54:57], off
	v_fmac_f32_e32 v85, v72, v72
	v_mul_f32_e32 v89, v50, v78
	v_mul_f32_e32 v54, 0x41c00000, v86
	v_mul_f32_e32 v55, 0x41c00000, v59
	v_mul_f32_e32 v56, 0x41c00000, v87
	v_mul_f32_e32 v57, 0x41c00000, v61
	v_add_f32_e32 v61, v80, v81
	v_med3_f32 v54, v54, s51, v177
	v_med3_f32 v55, v55, s51, v177
	v_med3_f32 v56, v56, s51, v177
	v_med3_f32 v57, v57, s51, v177
	v_add_f32_e32 v61, v61, v84
	v_add_f32_e32 v54, 0x4b400000, v54
	v_add_f32_e32 v55, 0x4b400000, v55
	v_add_f32_e32 v56, 0x4b400000, v56
	v_add_f32_e32 v57, 0x4b400000, v57
	v_add_f32_e32 v61, v85, v61
	v_perm_b32 v54, v55, v54, s56
	v_perm_b32 v55, v57, v56, s57
	v_add_f32_e32 v57, v88, v61
	v_or_b32_e32 v56, v54, v55
	ds_bpermute_b32 v54, v132, v57
	v_mul_f32_e32 v55, v53, v73
	v_mul_f32_e32 v55, 0x41c00000, v55
	v_mul_f32_e32 v79, v51, v79
	v_mul_f32_e32 v92, v52, v72
	v_med3_f32 v55, v55, s51, v177
	s_waitcnt lgkmcnt(0)
	v_add_f32_e32 v54, v57, v54
	v_mul_f32_e32 v58, 0x41c00000, v89
	v_mul_f32_e32 v59, 0x41c00000, v79
	v_mul_f32_e32 v60, 0x41c00000, v92
	v_add_f32_e32 v61, 0x4b400000, v55
	ds_bpermute_b32 v55, v133, v54
	v_med3_f32 v58, v58, s51, v177
	v_med3_f32 v59, v59, s51, v177
	v_med3_f32 v60, v60, s51, v177
	v_add_f32_e32 v58, 0x4b400000, v58
	v_add_f32_e32 v59, 0x4b400000, v59
	v_add_f32_e32 v60, 0x4b400000, v60
	v_perm_b32 v57, v59, v58, s56
	v_perm_b32 v58, v61, v60, s57
	v_or_b32_e32 v57, v57, v58
	global_store_dwordx2 v[70:71], v[56:57], off offset:128
	s_and_saveexec_b64 s[28:29], s[0:1]
	s_cbranch_execz .LBB0_627
	v_lshlrev_b64 v[56:57], 8, v[82:83]
	v_lshl_add_u64 v[56:57], s[22:23], 0, v[56:57]
	s_waitcnt lgkmcnt(0)
	v_add_f32_e32 v54, v54, v55
	global_store_dword v[56:57], v54, off
.LBB0_627:
	s_or_b64 exec, exec, s[28:29]
	s_add_u32 s98, s8, 0x280000
	s_addc_u32 s99, s9, 0
	global_load_dwordx4 v[228:231], v252, s[98:99] nt
	global_load_dwordx4 v[232:235], v252, s[98:99] offset:16 nt
	global_load_dwordx4 v[236:239], v252, s[98:99] offset:512 nt
	global_load_dwordx4 v[240:243], v252, s[98:99] offset:528 nt
	v_add_u32_e32 v54, 0x90, v140
	s_waitcnt lgkmcnt(0)
	v_ashrrev_i32_e32 v55, 31, v54
	v_lshlrev_b64 v[56:57], 12, v[54:55]
	v_lshl_add_u64 v[60:61], v[56:57], 0, v[138:139]
	v_lshl_add_u64 v[78:79], v[60:61], 2, s[8:9]
	s_nop 0
	s_nop 0
	v_cvt_f32_i32_e32 v47, v47
	v_cvt_f32_i32_e32 v46, v46
	v_cvt_f32_i32_e32 v49, v49
	v_cvt_f32_i32_e32 v48, v48
	v_cvt_f32_i32_e32 v81, v43
	v_cvt_f32_i32_e32 v80, v42
	v_cvt_f32_i32_e32 v45, v45
	v_cvt_f32_i32_e32 v44, v44
	v_lshlrev_b64 v[60:61], 1, v[60:61]
	v_lshl_add_u64 v[82:83], s[14:15], 0, v[60:61]
	v_mad_i64_i32 v[42:43], s[28:29], v54, s50, v[142:143]
	v_cvt_f32_i32_e32 v39, v39
	v_cvt_f32_i32_e32 v38, v38
	v_cvt_f32_i32_e32 v41, v41
	v_cvt_f32_i32_e32 v40, v40
	v_cvt_f32_i32_e32 v35, v35
	v_cvt_f32_i32_e32 v34, v34
	v_cvt_f32_i32_e32 v37, v37
	v_cvt_f32_i32_e32 v36, v36
	v_or_b32_e32 v60, 0x100, v60
	v_lshl_add_u64 v[60:61], s[14:15], 0, v[60:61]
	s_waitcnt vmcnt(8)
	v_pk_fma_f32 v[48:49], v[48:49], s[26:27], v[214:215] op_sel_hi:[1,0,1]
	v_pk_fma_f32 v[84:85], v[46:47], s[26:27], v[212:213] op_sel_hi:[1,0,1]
	s_waitcnt vmcnt(8)
	v_pk_fma_f32 v[72:73], v[44:45], s[26:27], v[218:219] op_sel_hi:[1,0,1]
	v_pk_fma_f32 v[70:71], v[80:81], s[26:27], v[216:217] op_sel_hi:[1,0,1]
	v_cvt_pk_bf16_f32 v44, v84, v85
	v_cvt_pk_bf16_f32 v45, v48, v49
	v_mul_f32_e32 v56, v74, v84
	v_cvt_pk_bf16_f32 v46, v70, v71
	v_cvt_pk_bf16_f32 v47, v72, v73
	v_mul_f32_e32 v57, v75, v85
	v_mul_f32_e32 v58, v76, v48
	v_mul_f32_e32 v59, v77, v49
	v_mul_f32_e32 v80, v66, v70
	v_mul_f32_e32 v81, v67, v71
	v_mul_f32_e32 v86, v68, v72
	v_mul_f32_e32 v87, v69, v73
	global_store_dwordx4 v[82:83], v[44:47], off
	v_mul_f32_e32 v49, v49, v49
	v_fmac_f32_e32 v49, v48, v48
	v_mul_f32_e32 v44, 0x41c00000, v56
	v_mul_f32_e32 v45, 0x41c00000, v57
	v_mul_f32_e32 v46, 0x41c00000, v58
	v_mul_f32_e32 v47, 0x41c00000, v59
	v_mul_f32_e32 v56, 0x41c00000, v80
	v_mul_f32_e32 v57, 0x41c00000, v81
	v_mul_f32_e32 v58, 0x41c00000, v86
	v_mul_f32_e32 v59, 0x41c00000, v87
	v_med3_f32 v44, v44, s51, v177
	v_med3_f32 v45, v45, s51, v177
	v_med3_f32 v46, v46, s51, v177
	v_med3_f32 v47, v47, s51, v177
	v_med3_f32 v56, v56, s51, v177
	v_med3_f32 v57, v57, s51, v177
	v_med3_f32 v58, v58, s51, v177
	v_med3_f32 v59, v59, s51, v177
	v_add_f32_e32 v44, 0x4b400000, v44
	v_add_f32_e32 v45, 0x4b400000, v45
	v_add_f32_e32 v46, 0x4b400000, v46
	v_add_f32_e32 v47, 0x4b400000, v47
	v_add_f32_e32 v56, 0x4b400000, v56
	v_add_f32_e32 v57, 0x4b400000, v57
	v_add_f32_e32 v58, 0x4b400000, v58
	v_add_f32_e32 v59, 0x4b400000, v59
	v_perm_b32 v44, v45, v44, s56
	v_perm_b32 v45, v47, v46, s57
	v_perm_b32 v46, v57, v56, s56
	v_perm_b32 v47, v59, v58, s57
	v_or_b32_e32 v44, v44, v45
	v_or_b32_e32 v45, v46, v47
	global_store_dwordx2 v[42:43], v[44:45], off
	s_nop 0
	s_nop 0
	s_nop 0
	v_mul_f32_e32 v78, v85, v85
	v_fmac_f32_e32 v78, v84, v84
	v_mul_f32_e32 v71, v71, v71
	v_add_f32_e32 v48, v78, v49
	v_fmac_f32_e32 v71, v70, v70
	v_mul_f32_e32 v73, v73, v73
	v_fmac_f32_e32 v73, v72, v72
	v_add_f32_e32 v48, v48, v71
	v_add_f32_e32 v48, v73, v48
	s_waitcnt vmcnt(11)
; __device__ __forceinline__ unsigned cvt_pk_bf16(float lo, float hi) { unsigned r; asm volatile("v_cvt_pk_bf16_f32 %0, %1, %2" : "=v"(r) : "v"(lo), "v"(hi)); return r; }
;     __device__ __forceinline__ void operator()(const f32x4 (&acc)[2][2][4][2], const Unit& u, int wr, int wc, int fr, int fq) const {
;     ...
;                 for (int bj = 0; bj < 2; ++bj) { const size_t off = r * 4096 + col0 + bj * HALF;
;                     const f32x4 v0 = acc[ai][bj][m][0] * scale + *(const f32x4*)(R + off), v1 = acc[ai][bj][m][1] * scale + *(const f32x4*)(R + off + 4);
;                     ss += (v0[0] * v0[0] + v0[1] * v0[1]) + (v0[2] * v0[2] + v0[3] * v0[3]) + (v1[0] * v1[0] + v1[1] * v1[1]) + (v1[2] * v1[2] + v1[3] * v1[3]);
;                     u32x4 w; w.x = cvt_pk_bf16(v0[0], v0[1]); w.y = cvt_pk_bf16(v0[2], v0[3]); w.z = cvt_pk_bf16(v1[0], v1[1]); w.w = cvt_pk_bf16(v1[2], v1[3]);
;                     *(u32x4*)(HB + off) = w;
;                     u32x2e q; q.x = q8x4(v0, gv[bj][0], (float)HQS); q.y = q8x4(v1, gv[bj][1], (float)HQS);
;                     *(u32x2e*)(Q8 + r * LDQ8 + col0 + bj * HALF) = q; }
;                 ss += __shfl_xor(ss, 16); ss += __shfl_xor(ss, 32);
;                 if (fq == 0) SSQP[r * 64 + u.pn * 4 + wc] = ss; }
	v_pk_fma_f32 v[40:41], v[40:41], s[26:27], v[222:223] op_sel_hi:[1,0,1]
	v_pk_fma_f32 v[38:39], v[38:39], s[26:27], v[220:221] op_sel_hi:[1,0,1]
	s_waitcnt vmcnt(11)
	v_pk_fma_f32 v[46:47], v[34:35], s[26:27], v[224:225] op_sel_hi:[1,0,1]
	v_mul_f32_e32 v49, v39, v39
	v_mul_f32_e32 v56, v41, v41
	v_pk_fma_f32 v[44:45], v[36:37], s[26:27], v[226:227] op_sel_hi:[1,0,1]
	v_mul_f32_e32 v57, v47, v47
	v_cvt_pk_bf16_f32 v34, v38, v39
	v_cvt_pk_bf16_f32 v35, v40, v41
	v_cvt_pk_bf16_f32 v36, v46, v47
	v_cvt_pk_bf16_f32 v37, v44, v45
	v_mul_f32_e32 v59, v62, v38
	v_mul_f32_e32 v39, v63, v39
	v_mul_f32_e32 v70, v64, v40
	v_mul_f32_e32 v41, v65, v41
	v_fmac_f32_e32 v49, v38, v38
	v_fmac_f32_e32 v56, v40, v40
	v_mul_f32_e32 v58, v45, v45
	v_fmac_f32_e32 v57, v46, v46
	global_store_dwordx4 v[60:61], v[34:37], off
	v_fmac_f32_e32 v58, v44, v44
	v_mul_f32_e32 v71, v50, v46
	v_mul_f32_e32 v34, 0x41c00000, v59
	v_mul_f32_e32 v35, 0x41c00000, v39
	v_mul_f32_e32 v36, 0x41c00000, v70
	v_mul_f32_e32 v37, 0x41c00000, v41
	v_add_f32_e32 v41, v49, v56
	v_med3_f32 v34, v34, s51, v177
	v_med3_f32 v35, v35, s51, v177
	v_med3_f32 v36, v36, s51, v177
	v_med3_f32 v37, v37, s51, v177
	v_add_f32_e32 v41, v41, v57
	v_add_f32_e32 v34, 0x4b400000, v34
	v_add_f32_e32 v35, 0x4b400000, v35
	v_add_f32_e32 v36, 0x4b400000, v36
	v_add_f32_e32 v37, 0x4b400000, v37
	v_add_f32_e32 v41, v58, v41
	v_perm_b32 v34, v35, v34, s56
	v_perm_b32 v35, v37, v36, s57
	v_add_f32_e32 v37, v48, v41
	v_or_b32_e32 v36, v34, v35
	ds_bpermute_b32 v34, v132, v37
	v_mul_f32_e32 v35, v53, v45
	v_mul_f32_e32 v35, 0x41c00000, v35
	v_mul_f32_e32 v47, v51, v47
	v_mul_f32_e32 v72, v52, v44
	v_med3_f32 v35, v35, s51, v177
	s_waitcnt lgkmcnt(0)
	v_add_f32_e32 v34, v37, v34
	v_mul_f32_e32 v38, 0x41c00000, v71
	v_mul_f32_e32 v39, 0x41c00000, v47
	v_mul_f32_e32 v40, 0x41c00000, v72
	v_add_f32_e32 v41, 0x4b400000, v35
	ds_bpermute_b32 v35, v133, v34
	v_med3_f32 v38, v38, s51, v177
	v_med3_f32 v39, v39, s51, v177
	v_med3_f32 v40, v40, s51, v177
	v_add_f32_e32 v38, 0x4b400000, v38
	v_add_f32_e32 v39, 0x4b400000, v39
	v_add_f32_e32 v40, 0x4b400000, v40
	v_perm_b32 v37, v39, v38, s56
	v_perm_b32 v38, v41, v40, s57
	v_or_b32_e32 v37, v37, v38
	global_store_dwordx2 v[42:43], v[36:37], off offset:128
	s_and_saveexec_b64 s[28:29], s[0:1]
	s_cbranch_execz .LBB0_629
	v_lshlrev_b64 v[36:37], 8, v[54:55]
	v_lshl_add_u64 v[36:37], s[22:23], 0, v[36:37]
	s_waitcnt lgkmcnt(0)
	v_add_f32_e32 v34, v34, v35
	global_store_dword v[36:37], v34, off
; __device__ __forceinline__ unsigned cvt_pk_bf16(float lo, float hi) { unsigned r; asm volatile("v_cvt_pk_bf16_f32 %0, %1, %2" : "=v"(r) : "v"(lo), "v"(hi)); return r; }
;     __device__ __forceinline__ void operator()(const f32x4 (&acc)[2][2][4][2], const Unit& u, int wr, int wc, int fr, int fq) const {
;     ...
;             for (int m = 0; m < 4; ++m) { const size_t r = (size_t)(row0 + ai * HALF + m * 16); float ss = 0.f;
; #pragma unroll
;                 for (int bj = 0; bj < 2; ++bj) { const size_t off = r * 4096 + col0 + bj * HALF;
;                     const f32x4 v0 = acc[ai][bj][m][0] * scale + *(const f32x4*)(R + off), v1 = acc[ai][bj][m][1] * scale + *(const f32x4*)(R + off + 4);
;                     ss += (v0[0] * v0[0] + v0[1] * v0[1]) + (v0[2] * v0[2] + v0[3] * v0[3]) + (v1[0] * v1[0] + v1[1] * v1[1]) + (v1[2] * v1[2] + v1[3] * v1[3]);
;                     u32x4 w; w.x = cvt_pk_bf16(v0[0], v0[1]); w.y = cvt_pk_bf16(v0[2], v0[3]); w.z = cvt_pk_bf16(v1[0], v1[1]); w.w = cvt_pk_bf16(v1[2], v1[3]);
;                     *(u32x4*)(HB + off) = w;
;                     u32x2e q; q.x = q8x4(v0, gv[bj][0], (float)HQS); q.y = q8x4(v1, gv[bj][1], (float)HQS);
;                     *(u32x2e*)(Q8 + r * LDQ8 + col0 + bj * HALF) = q; }
;                 ss += __shfl_xor(ss, 16); ss += __shfl_xor(ss, 32);
;                 if (fq == 0) SSQP[r * 64 + u.pn * 4 + wc] = ss; }
.LBB0_629:
	s_or_b64 exec, exec, s[28:29]
	s_add_u32 s98, s8, 0x2c0000
	s_addc_u32 s99, s9, 0
	global_load_dwordx4 v[212:215], v252, s[98:99] nt
	global_load_dwordx4 v[216:219], v252, s[98:99] offset:16 nt
	global_load_dwordx4 v[220:223], v252, s[98:99] offset:512 nt
	global_load_dwordx4 v[224:227], v252, s[98:99] offset:528 nt
	v_add_u32_e32 v34, 0xa0, v140
	s_waitcnt lgkmcnt(0)
	v_ashrrev_i32_e32 v35, 31, v34
	v_lshlrev_b64 v[36:37], 12, v[34:35]
	v_lshl_add_u64 v[44:45], v[36:37], 0, v[138:139]
	v_lshl_add_u64 v[46:47], v[44:45], 2, s[8:9]
	s_nop 0
	s_nop 0
	v_cvt_f32_i32_e32 v31, v31
	v_cvt_f32_i32_e32 v30, v30
	v_cvt_f32_i32_e32 v33, v33
	v_cvt_f32_i32_e32 v32, v32
	v_cvt_f32_i32_e32 v49, v27
	v_cvt_f32_i32_e32 v48, v26
	v_cvt_f32_i32_e32 v29, v29
	v_cvt_f32_i32_e32 v28, v28
	v_lshlrev_b64 v[44:45], 1, v[44:45]
	v_lshl_add_u64 v[54:55], s[14:15], 0, v[44:45]
	v_mad_i64_i32 v[26:27], s[28:29], v34, s50, v[142:143]
	v_cvt_f32_i32_e32 v23, v23
	v_cvt_f32_i32_e32 v22, v22
	v_cvt_f32_i32_e32 v25, v25
	v_cvt_f32_i32_e32 v24, v24
	v_cvt_f32_i32_e32 v19, v19
	v_cvt_f32_i32_e32 v18, v18
	v_cvt_f32_i32_e32 v21, v21
	v_cvt_f32_i32_e32 v20, v20
	v_or_b32_e32 v44, 0x100, v44
	v_lshl_add_u64 v[44:45], s[14:15], 0, v[44:45]
	s_waitcnt vmcnt(8)
	v_pk_fma_f32 v[32:33], v[32:33], s[26:27], v[230:231] op_sel_hi:[1,0,1]
	v_pk_fma_f32 v[56:57], v[30:31], s[26:27], v[228:229] op_sel_hi:[1,0,1]
	s_waitcnt vmcnt(8)
	v_pk_fma_f32 v[42:43], v[28:29], s[26:27], v[234:235] op_sel_hi:[1,0,1]
	v_pk_fma_f32 v[40:41], v[48:49], s[26:27], v[232:233] op_sel_hi:[1,0,1]
	v_cvt_pk_bf16_f32 v28, v56, v57
	v_cvt_pk_bf16_f32 v29, v32, v33
	v_mul_f32_e32 v36, v74, v56
	v_cvt_pk_bf16_f32 v30, v40, v41
	v_cvt_pk_bf16_f32 v31, v42, v43
	v_mul_f32_e32 v37, v75, v57
	v_mul_f32_e32 v38, v76, v32
	v_mul_f32_e32 v39, v77, v33
	v_mul_f32_e32 v48, v66, v40
	v_mul_f32_e32 v49, v67, v41
	v_mul_f32_e32 v58, v68, v42
	v_mul_f32_e32 v59, v69, v43
	global_store_dwordx4 v[54:55], v[28:31], off
	v_mul_f32_e32 v33, v33, v33
	v_fmac_f32_e32 v33, v32, v32
	v_mul_f32_e32 v28, 0x41c00000, v36
	v_mul_f32_e32 v29, 0x41c00000, v37
	v_mul_f32_e32 v30, 0x41c00000, v38
	v_mul_f32_e32 v31, 0x41c00000, v39
	v_mul_f32_e32 v36, 0x41c00000, v48
	v_mul_f32_e32 v37, 0x41c00000, v49
	v_mul_f32_e32 v38, 0x41c00000, v58
	v_mul_f32_e32 v39, 0x41c00000, v59
	v_med3_f32 v28, v28, s51, v177
	v_med3_f32 v29, v29, s51, v177
	v_med3_f32 v30, v30, s51, v177
	v_med3_f32 v31, v31, s51, v177
	v_med3_f32 v36, v36, s51, v177
	v_med3_f32 v37, v37, s51, v177
	v_med3_f32 v38, v38, s51, v177
	v_med3_f32 v39, v39, s51, v177
	v_add_f32_e32 v28, 0x4b400000, v28
	v_add_f32_e32 v29, 0x4b400000, v29
	v_add_f32_e32 v30, 0x4b400000, v30
	v_add_f32_e32 v31, 0x4b400000, v31
	v_add_f32_e32 v36, 0x4b400000, v36
	v_add_f32_e32 v37, 0x4b400000, v37
	v_add_f32_e32 v38, 0x4b400000, v38
	v_add_f32_e32 v39, 0x4b400000, v39
	v_perm_b32 v28, v29, v28, s56
	v_perm_b32 v29, v31, v30, s57
	v_perm_b32 v30, v37, v36, s56
	v_perm_b32 v31, v39, v38, s57
	v_or_b32_e32 v28, v28, v29
	v_or_b32_e32 v29, v30, v31
	global_store_dwordx2 v[26:27], v[28:29], off
	s_nop 0
	s_nop 0
	s_nop 0
	v_mul_f32_e32 v46, v57, v57
	v_fmac_f32_e32 v46, v56, v56
	v_mul_f32_e32 v41, v41, v41
	v_add_f32_e32 v32, v46, v33
	v_fmac_f32_e32 v41, v40, v40
	v_mul_f32_e32 v43, v43, v43
	v_fmac_f32_e32 v43, v42, v42
	v_add_f32_e32 v32, v32, v41
	v_add_f32_e32 v32, v43, v32
	s_waitcnt vmcnt(11)
	v_pk_fma_f32 v[24:25], v[24:25], s[26:27], v[238:239] op_sel_hi:[1,0,1]
	v_pk_fma_f32 v[22:23], v[22:23], s[26:27], v[236:237] op_sel_hi:[1,0,1]
	s_waitcnt vmcnt(11)
	v_pk_fma_f32 v[30:31], v[18:19], s[26:27], v[240:241] op_sel_hi:[1,0,1]
	v_mul_f32_e32 v33, v23, v23
	v_mul_f32_e32 v36, v25, v25
	v_pk_fma_f32 v[28:29], v[20:21], s[26:27], v[242:243] op_sel_hi:[1,0,1]
	v_mul_f32_e32 v37, v31, v31
	v_cvt_pk_bf16_f32 v18, v22, v23
	v_cvt_pk_bf16_f32 v19, v24, v25
	v_cvt_pk_bf16_f32 v20, v30, v31
	v_cvt_pk_bf16_f32 v21, v28, v29
	v_mul_f32_e32 v39, v62, v22
	v_mul_f32_e32 v23, v63, v23
	v_mul_f32_e32 v40, v64, v24
	v_mul_f32_e32 v25, v65, v25
	v_fmac_f32_e32 v33, v22, v22
	v_fmac_f32_e32 v36, v24, v24
	v_mul_f32_e32 v38, v29, v29
	v_fmac_f32_e32 v37, v30, v30
	global_store_dwordx4 v[44:45], v[18:21], off
	v_fmac_f32_e32 v38, v28, v28
	v_mul_f32_e32 v41, v50, v30
	v_mul_f32_e32 v18, 0x41c00000, v39
	v_mul_f32_e32 v19, 0x41c00000, v23
	v_mul_f32_e32 v20, 0x41c00000, v40
	v_mul_f32_e32 v21, 0x41c00000, v25
	v_add_f32_e32 v25, v33, v36
	v_med3_f32 v18, v18, s51, v177
	v_med3_f32 v19, v19, s51, v177
	v_med3_f32 v20, v20, s51, v177
	v_med3_f32 v21, v21, s51, v177
	v_add_f32_e32 v25, v25, v37
	v_add_f32_e32 v18, 0x4b400000, v18
	v_add_f32_e32 v19, 0x4b400000, v19
	v_add_f32_e32 v20, 0x4b400000, v20
	v_add_f32_e32 v21, 0x4b400000, v21
	v_add_f32_e32 v25, v38, v25
	v_perm_b32 v18, v19, v18, s56
	v_perm_b32 v19, v21, v20, s57
	v_add_f32_e32 v21, v32, v25
	v_or_b32_e32 v20, v18, v19
	ds_bpermute_b32 v18, v132, v21
	v_mul_f32_e32 v19, v53, v29
	v_mul_f32_e32 v19, 0x41c00000, v19
	v_mul_f32_e32 v31, v51, v31
	v_mul_f32_e32 v42, v52, v28
	v_med3_f32 v19, v19, s51, v177
	s_waitcnt lgkmcnt(0)
	v_add_f32_e32 v18, v21, v18
	v_mul_f32_e32 v22, 0x41c00000, v41
	v_mul_f32_e32 v23, 0x41c00000, v31
	v_mul_f32_e32 v24, 0x41c00000, v42
	v_add_f32_e32 v25, 0x4b400000, v19
	ds_bpermute_b32 v19, v133, v18
	v_med3_f32 v22, v22, s51, v177
	v_med3_f32 v23, v23, s51, v177
	v_med3_f32 v24, v24, s51, v177
	v_add_f32_e32 v22, 0x4b400000, v22
	v_add_f32_e32 v23, 0x4b400000, v23
	v_add_f32_e32 v24, 0x4b400000, v24
	v_perm_b32 v21, v23, v22, s56
	v_perm_b32 v22, v25, v24, s57
	v_or_b32_e32 v21, v21, v22
	global_store_dwordx2 v[26:27], v[20:21], off offset:128
	s_and_saveexec_b64 s[28:29], s[0:1]
	s_cbranch_execz .LBB0_631
	v_lshlrev_b64 v[20:21], 8, v[34:35]
	v_lshl_add_u64 v[20:21], s[22:23], 0, v[20:21]
	s_waitcnt lgkmcnt(0)
	v_add_f32_e32 v18, v18, v19
	global_store_dword v[20:21], v18, off

; #define LAS __attribute__((address_space(3)))
; #define LDS_WAIT() asm volatile("s_waitcnt lgkmcnt(0)" ::: "memory")
; template <int TPS> __device__ __forceinline__ int p9_build_desc(const int* BST, int tb, int lane, LAS int* DS) {
;     const int tkg = lane & (TPS - 1), bg = (lane / TPS) & 7; const int s0 = BST[(size_t)(tb + tkg) * 16 + bg], s1 = BST[(size_t)(tb + tkg) * 16 + bg + 1], cnt = lane < 8 * TPS ? s1 - s0 : 0, nb = (cnt + 7) >> 3;
;     int inc = nb;
; #pragma unroll
;     for (int o = 1; o < 64; o <<= 1) { const int v = __shfl_up(inc, o); inc += (lane >= o) ? v : 0; }
;     const int off = inc - nb, NBT = __builtin_amdgcn_readlane(inc, 63);
;     for (int i = 0; i < nb; ++i) DS[off + i] = tkg | ((s0 + 8 * i) << 3) | (imin(8, cnt - 8 * i) << 10);
;     const int NBP = ((NBT + 2) / 3) * 3;
;     if (lane < NBP + 2 - NBT) DS[NBT + lane] = 0;
;     LDS_WAIT();
.LBB0_860:
	s_or_b64 exec, exec, s[18:19]
	s_add_i32 s18, s50, 2
	s_mul_hi_i32 s18, s18, 0x55555556
	s_lshr_b32 s19, s18, 31
	s_add_i32 s23, s18, s19
	s_mul_i32 s23, s23, 3
	s_sub_i32 s18, s23, s50
	s_add_i32 s18, s18, 2
	v_cmp_gt_i32_e32 vcc, s18, v202
	s_and_saveexec_b64 s[18:19], vcc
	v_lshl_add_u32 v32, s50, 2, v145
	ds_write_b32 v32, v128 offset:8192
	s_or_b64 exec, exec, s[18:19]
	s_waitcnt lgkmcnt(0)
	v_mov_b32_e32 v32, s33
	ds_read_b64 v[32:33], v32 offset:8192
	s_waitcnt lgkmcnt(0)
	v_readfirstlane_b32 s18, v32
	s_lshl_b32 s42, s18, 9
	s_ashr_i32 s19, s18, 10
	s_and_b32 s42, s42, 0xe00
	s_lshr_b32 s18, s18, 1
	s_max_i32 s19, s19, 1
	s_add_i32 s42, s33, s42
	s_and_b32 s18, s18, 0x1fc
	s_add_i32 s19, s19, -1
	s_add_i32 s42, s42, s18
	v_readfirstlane_b32 s18, v33
	v_min_u32_e32 v32, s19, v134
	s_ashr_i32 s19, s18, 10
	s_max_i32 s19, s19, 1
	s_add_i32 s19, s19, -1
	v_min_i32_e32 v33, s19, v134
	s_lshl_b32 s19, s18, 9
	s_and_b32 s19, s19, 0xe00
	s_lshr_b32 s18, s18, 1
	s_add_i32 s19, s33, s19
	s_and_b32 s18, s18, 0x1fc
	s_add_i32 s19, s19, s18
	v_lshl_add_u32 v32, v32, 2, s42
	v_lshl_add_u32 v33, v33, 2, s19
	ds_read_b32 v32, v32
	ds_read_b32 v33, v33
	s_cmp_lt_i32 s23, 1
	s_waitcnt lgkmcnt(1)
	v_readlane_b32 s18, v32, 0
	v_readlane_b32 s42, v32, 1
	v_readlane_b32 s44, v32, 2
	v_readlane_b32 s46, v32, 3
	v_readlane_b32 s48, v32, 4
	v_readlane_b32 s50, v32, 5
	v_readlane_b32 s52, v32, 6
	v_readlane_b32 s56, v32, 7
	s_waitcnt lgkmcnt(0)
	v_readlane_b32 s58, v33, 0
	v_readlane_b32 s60, v33, 1
	v_readlane_b32 s68, v33, 2
	v_readlane_b32 s70, v33, 3
	v_readlane_b32 s72, v33, 4
	v_readlane_b32 s74, v33, 5
	v_readlane_b32 s76, v33, 6
	v_readlane_b32 s78, v33, 7
	s_cbranch_scc1 .LBB0_846
	s_ashr_i32 s19, s18, 31
	s_ashr_i32 s43, s42, 31
	s_ashr_i32 s45, s44, 31
	s_ashr_i32 s47, s46, 31
	s_ashr_i32 s49, s48, 31
	s_ashr_i32 s51, s50, 31
	s_ashr_i32 s53, s52, 31
	s_ashr_i32 s57, s56, 31
	s_lshl_b64 s[18:19], s[18:19], 10
	s_lshl_b64 s[42:43], s[42:43], 10
	s_lshl_b64 s[44:45], s[44:45], 10
	s_lshl_b64 s[46:47], s[46:47], 10
	s_lshl_b64 s[48:49], s[48:49], 10
	s_lshl_b64 s[50:51], s[50:51], 10
	s_lshl_b64 s[52:53], s[52:53], 10
	s_lshl_b64 s[56:57], s[56:57], 10
	v_lshl_add_u64 v[92:93], v[130:131], 0, s[18:19]
	v_lshl_add_u64 v[88:89], v[130:131], 0, s[42:43]
	v_lshl_add_u64 v[84:85], v[130:131], 0, s[44:45]
	v_lshl_add_u64 v[80:81], v[130:131], 0, s[46:47]
	v_lshl_add_u64 v[76:77], v[130:131], 0, s[48:49]
	v_lshl_add_u64 v[68:69], v[130:131], 0, s[50:51]
	v_lshl_add_u64 v[60:61], v[130:131], 0, s[52:53]
	v_lshl_add_u64 v[52:53], v[130:131], 0, s[56:57]
	global_load_dwordx4 v[92:95], v[92:93], off
	s_nop 0
	global_load_dwordx4 v[88:91], v[88:89], off
	s_nop 0
	global_load_dwordx4 v[84:87], v[84:85], off
	s_nop 0
	global_load_dwordx4 v[80:83], v[80:81], off
	s_nop 0
	global_load_dwordx4 v[76:79], v[76:77], off
	s_nop 0
	global_load_dwordx4 v[68:71], v[68:69], off
	s_nop 0
	global_load_dwordx4 v[60:63], v[60:61], off
	s_nop 0
	global_load_dwordx4 v[52:55], v[52:53], off
	s_nop 0
	s_ashr_i32 s59, s58, 31
	s_ashr_i32 s61, s60, 31
	s_ashr_i32 s69, s68, 31
	s_ashr_i32 s71, s70, 31
	s_ashr_i32 s73, s72, 31
	s_ashr_i32 s75, s74, 31
	s_ashr_i32 s77, s76, 31
	s_ashr_i32 s79, s78, 31
	s_lshl_b64 s[58:59], s[58:59], 10
	s_lshl_b64 s[60:61], s[60:61], 10
	s_lshl_b64 s[68:69], s[68:69], 10
	s_lshl_b64 s[70:71], s[70:71], 10
	s_lshl_b64 s[72:73], s[72:73], 10
	s_lshl_b64 s[74:75], s[74:75], 10
	s_lshl_b64 s[76:77], s[76:77], 10
	s_lshl_b64 s[78:79], s[78:79], 10
	v_lshl_add_u64 v[72:73], v[130:131], 0, s[58:59]
	v_lshl_add_u64 v[64:65], v[130:131], 0, s[60:61]
	v_lshl_add_u64 v[56:57], v[130:131], 0, s[68:69]
	v_lshl_add_u64 v[48:49], v[130:131], 0, s[70:71]
	v_lshl_add_u64 v[44:45], v[130:131], 0, s[72:73]
	v_lshl_add_u64 v[40:41], v[130:131], 0, s[74:75]
	v_lshl_add_u64 v[36:37], v[130:131], 0, s[76:77]
	v_lshl_add_u64 v[32:33], v[130:131], 0, s[78:79]
	global_load_dwordx4 v[72:75], v[72:73], off
	s_nop 0
	global_load_dwordx4 v[64:67], v[64:65], off
	s_nop 0
	global_load_dwordx4 v[56:59], v[56:57], off
	s_nop 0
	global_load_dwordx4 v[48:51], v[48:49], off
	s_nop 0
	global_load_dwordx4 v[44:47], v[44:45], off
	s_nop 0
	global_load_dwordx4 v[40:43], v[40:41], off
	s_nop 0
	global_load_dwordx4 v[36:39], v[36:37], off
	s_nop 0
	global_load_dwordx4 v[32:35], v[32:33], off
	s_nop 0
	s_mov_b32 s58, 0
	s_mov_b32 s59, s80
	s_branch .LBB0_866

; __device__ __forceinline__ int ifold32(int a, int b) { const auto r = __builtin_amdgcn_permlane32_swap((unsigned)a, (unsigned)b, false, false); return (int)(r[0] + r[1]); }
; __device__ __forceinline__ int ifold16(int a, int b) { const auto r = __builtin_amdgcn_permlane16_swap((unsigned)a, (unsigned)b, false, false); return (int)(r[0] + r[1]); }
; template <int CTRL> __device__ __forceinline__ int idppadd(int v) { return v + __builtin_amdgcn_update_dpp(0, v, CTRL, 0xf, 0xf, false); }
.LBB0_866:
	s_waitcnt vmcnt(16)
	v_mov_b32_e32 v96, s59
	ds_read2_b32 v[142:143], v96 offset1:2
	s_mov_b32 s60, s59
	s_waitcnt lgkmcnt(0)
	v_readfirstlane_b32 s18, v143
	s_ashr_i32 s19, s18, 10
	s_lshl_b32 s42, s18, 9
	s_lshr_b32 s18, s18, 1
	s_max_i32 s19, s19, 1
	s_and_b32 s42, s42, 0xe00
	s_add_i32 s19, s19, -1
	s_add_i32 s42, s33, s42
	s_and_b32 s18, s18, 0x1fc
	v_min_i32_e32 v96, s19, v134
	s_add_i32 s42, s42, s18
	v_lshl_add_u32 v96, v96, 2, s42
	ds_read_b32 v96, v96
	v_readfirstlane_b32 s59, v142
	s_waitcnt lgkmcnt(0)
	v_readlane_b32 s56, v96, 0
	v_readlane_b32 s52, v96, 1
	v_readlane_b32 s50, v96, 2
	v_readlane_b32 s48, v96, 3
	s_ashr_i32 s57, s56, 31
	s_ashr_i32 s53, s52, 31
	v_readlane_b32 s46, v96, 4
	v_readlane_b32 s44, v96, 5
	s_lshl_b64 s[56:57], s[56:57], 10
	s_lshl_b64 s[52:53], s[52:53], 10
	s_ashr_i32 s51, s50, 31
	s_ashr_i32 s49, s48, 31
	v_readlane_b32 s42, v96, 6
	v_readlane_b32 s18, v96, 7
	v_lshl_add_u64 v[96:97], v[130:131], 0, s[56:57]
	v_lshl_add_u64 v[98:99], v[130:131], 0, s[52:53]
	s_lshl_b64 s[50:51], s[50:51], 10
	s_lshl_b64 s[48:49], s[48:49], 10
	s_ashr_i32 s47, s46, 31
	s_ashr_i32 s45, s44, 31
	global_load_dwordx4 v[124:127], v[96:97], off
	global_load_dwordx4 v[116:119], v[98:99], off
	v_lshl_add_u64 v[96:97], v[130:131], 0, s[50:51]
	v_lshl_add_u64 v[98:99], v[130:131], 0, s[48:49]
	s_lshl_b64 s[46:47], s[46:47], 10
	s_lshl_b64 s[44:45], s[44:45], 10
	s_ashr_i32 s43, s42, 31
	s_ashr_i32 s19, s18, 31
	global_load_dwordx4 v[120:123], v[96:97], off
	global_load_dwordx4 v[108:111], v[98:99], off
	v_lshl_add_u64 v[96:97], v[130:131], 0, s[46:47]
	v_lshl_add_u64 v[98:99], v[130:131], 0, s[44:45]
	s_lshl_b64 s[42:43], s[42:43], 10
	s_lshl_b64 s[18:19], s[18:19], 10
	global_load_dwordx4 v[112:115], v[96:97], off
	global_load_dwordx4 v[100:103], v[98:99], off
	v_lshl_add_u64 v[96:97], v[130:131], 0, s[42:43]
	v_lshl_add_u64 v[98:99], v[130:131], 0, s[18:19]
	global_load_dwordx4 v[104:107], v[96:97], off
	s_nop 0
	global_load_dwordx4 v[96:99], v[98:99], off
	s_ashr_i32 s44, s59, 10
	s_and_b32 s45, s59, 7
	s_bfe_u32 s42, s59, 0x70003
	s_max_i32 s43, s44, 1
	s_cmp_lt_i32 s45, 4
	s_mov_b64 s[18:19], -1
	s_cbranch_scc1 .LBB0_887
	s_cmp_lt_i32 s45, 6
	s_cbranch_scc1 .LBB0_877
	s_cmp_gt_i32 s45, 6
	s_cbranch_scc0 .LBB0_872
	v_mov_b32_e32 v154, 0
	s_waitcnt vmcnt(16)
	v_dot4c_i32_i8_e32 v154, v91, v27
	v_mov_b32_e32 v155, 0
	v_dot4c_i32_i8_e32 v154, v90, v26
	v_dot4c_i32_i8_e32 v155, v87, v27
	v_mov_b32_e32 v156, 0
	s_cmp_gt_i32 s44, 1
	v_dot4c_i32_i8_e32 v154, v89, v25
	v_dot4c_i32_i8_e32 v155, v86, v26
	v_dot4c_i32_i8_e32 v156, v83, v27
	v_mov_b32_e32 v157, 0
	v_dot4c_i32_i8_e32 v154, v88, v24
	s_cselect_b64 vcc, -1, 0
	s_cmp_gt_i32 s44, 2
	v_dot4c_i32_i8_e32 v155, v85, v25
	v_dot4c_i32_i8_e32 v156, v82, v26
	v_dot4c_i32_i8_e32 v157, v79, v27
	v_mov_b32_e32 v158, 0
	v_cndmask_b32_e32 v154, 0, v154, vcc
	v_dot4c_i32_i8_e32 v155, v84, v24
	s_cselect_b64 vcc, -1, 0
	s_cmp_gt_i32 s44, 3
	v_dot4c_i32_i8_e32 v156, v81, v25
	v_dot4c_i32_i8_e32 v157, v78, v26
	v_dot4c_i32_i8_e32 v158, v71, v27
	v_mov_b32_e32 v159, 0
	v_cndmask_b32_e32 v155, 0, v155, vcc
	v_dot4c_i32_i8_e32 v156, v80, v24
	s_cselect_b64 vcc, -1, 0
	s_cmp_gt_i32 s44, 4
	v_dot4c_i32_i8_e32 v157, v77, v25
	v_dot4c_i32_i8_e32 v158, v70, v26
	v_dot4c_i32_i8_e32 v159, v63, v27
	v_mov_b32_e32 v160, 0
	v_mov_b32_e32 v142, 0
	v_cndmask_b32_e32 v156, 0, v156, vcc
	v_dot4c_i32_i8_e32 v157, v76, v24
	s_cselect_b64 vcc, -1, 0
	s_cmp_gt_i32 s44, 5
	v_dot4c_i32_i8_e32 v158, v69, v25
	v_dot4c_i32_i8_e32 v159, v62, v26
	v_dot4c_i32_i8_e32 v160, v55, v27
	s_waitcnt vmcnt(16)
	v_dot4c_i32_i8_e32 v142, v95, v27
	v_cndmask_b32_e32 v157, 0, v157, vcc
	v_dot4c_i32_i8_e32 v158, v68, v24
	s_cselect_b64 vcc, -1, 0
	s_cmp_gt_i32 s44, 6
	v_dot4c_i32_i8_e32 v159, v61, v25
	v_dot4c_i32_i8_e32 v160, v54, v26
	v_dot4c_i32_i8_e32 v142, v94, v26
	v_cndmask_b32_e32 v158, 0, v158, vcc
	v_dot4c_i32_i8_e32 v159, v60, v24
	s_cselect_b64 vcc, -1, 0
	s_cmp_gt_i32 s44, 7
	v_dot4c_i32_i8_e32 v160, v53, v25
	v_dot4c_i32_i8_e32 v142, v93, v25
	v_cndmask_b32_e32 v159, 0, v159, vcc
	v_dot4c_i32_i8_e32 v160, v52, v24
	s_cselect_b64 vcc, -1, 0
	v_dot4c_i32_i8_e32 v142, v92, v24
	v_permlane32_swap_b32_e32 v155, v156
	v_cndmask_b32_e32 v160, 0, v160, vcc
	s_nop 0
	v_permlane32_swap_b32_e32 v142, v154
	v_permlane32_swap_b32_e32 v157, v158
	v_permlane32_swap_b32_e32 v159, v160
	v_add_u32_e32 v142, v142, v154
	v_add_u32_e32 v154, v155, v156
	v_add_u32_e32 v155, v157, v158
	v_add_u32_e32 v156, v159, v160
	v_permlane16_swap_b32_e32 v142, v154
	s_nop 0
	v_permlane16_swap_b32_e32 v155, v156
	v_add_u32_e32 v142, v142, v154
	v_add_u32_e32 v154, v155, v156
	v_cndmask_b32_e64 v155, v154, v142, s[14:15]
	v_cndmask_b32_e64 v142, v142, v154, s[14:15]
	v_mov_b32_e32 v154, 0
	v_cmp_gt_u32_e32 vcc, s43, v144
	v_add_u32_dpp v142, v142, v155 row_ror:8 row_mask:0xf bank_mask:0xf bound_ctrl:1
	s_and_b64 s[46:47], s[16:17], vcc
	s_nop 0
	v_add_u32_dpp v142, v142, v142 quad_perm:[1,0,3,2] row_mask:0xf bank_mask:0xf bound_ctrl:1
	s_nop 1
	v_add_u32_dpp v142, v142, v142 quad_perm:[2,3,0,1] row_mask:0xf bank_mask:0xf bound_ctrl:1
	s_nop 1
	v_mov_b32_dpp v154, v142 row_half_mirror row_mask:0xf bank_mask:0xf
	s_and_saveexec_b64 s[18:19], s[46:47]
	s_cbranch_execz .LBB0_871
	v_add_u32_e32 v142, v142, v154
	v_cvt_f32_i32_e32 v142, v142
	v_lshl_add_u32 v154, s42, 2, v152
	v_mul_f32_e32 v142, 0x382aaaab, v142
	ds_write_b32 v154, v142 offset:7680

; __device__ __forceinline__ int ifold32(int a, int b) { const auto r = __builtin_amdgcn_permlane32_swap((unsigned)a, (unsigned)b, false, false); return (int)(r[0] + r[1]); }
; __device__ __forceinline__ int ifold16(int a, int b) { const auto r = __builtin_amdgcn_permlane16_swap((unsigned)a, (unsigned)b, false, false); return (int)(r[0] + r[1]); }
; template <int CTRL> __device__ __forceinline__ int idppadd(int v) { return v + __builtin_amdgcn_update_dpp(0, v, CTRL, 0xf, 0xf, false); }
.LBB0_872:
	s_andn2_b64 vcc, exec, s[18:19]
	s_cbranch_vccnz .LBB0_876
	v_mov_b32_e32 v154, 0
	s_waitcnt vmcnt(16)
	v_dot4c_i32_i8_e32 v154, v91, v31
	v_mov_b32_e32 v155, 0
	v_dot4c_i32_i8_e32 v154, v90, v30
	v_dot4c_i32_i8_e32 v155, v87, v31
	v_mov_b32_e32 v156, 0
	s_cmp_gt_i32 s44, 1
	v_dot4c_i32_i8_e32 v154, v89, v29
	v_dot4c_i32_i8_e32 v155, v86, v30
	v_dot4c_i32_i8_e32 v156, v83, v31
	v_mov_b32_e32 v157, 0
	v_dot4c_i32_i8_e32 v154, v88, v28
	s_cselect_b64 vcc, -1, 0
	s_cmp_gt_i32 s44, 2
	v_dot4c_i32_i8_e32 v155, v85, v29
	v_dot4c_i32_i8_e32 v156, v82, v30
	v_dot4c_i32_i8_e32 v157, v79, v31
	v_mov_b32_e32 v158, 0
	v_cndmask_b32_e32 v154, 0, v154, vcc
	v_dot4c_i32_i8_e32 v155, v84, v28
	s_cselect_b64 vcc, -1, 0
	s_cmp_gt_i32 s44, 3
	v_dot4c_i32_i8_e32 v156, v81, v29
	v_dot4c_i32_i8_e32 v157, v78, v30
	v_dot4c_i32_i8_e32 v158, v71, v31
	v_mov_b32_e32 v159, 0
	v_cndmask_b32_e32 v155, 0, v155, vcc
	v_dot4c_i32_i8_e32 v156, v80, v28
	s_cselect_b64 vcc, -1, 0
	s_cmp_gt_i32 s44, 4
	v_dot4c_i32_i8_e32 v157, v77, v29
	v_dot4c_i32_i8_e32 v158, v70, v30
	v_dot4c_i32_i8_e32 v159, v63, v31
	v_mov_b32_e32 v160, 0
	v_mov_b32_e32 v142, 0
	v_cndmask_b32_e32 v156, 0, v156, vcc
	v_dot4c_i32_i8_e32 v157, v76, v28
	s_cselect_b64 vcc, -1, 0
	s_cmp_gt_i32 s44, 5
	v_dot4c_i32_i8_e32 v158, v69, v29
	v_dot4c_i32_i8_e32 v159, v62, v30
	v_dot4c_i32_i8_e32 v160, v55, v31
	s_waitcnt vmcnt(16)
	v_dot4c_i32_i8_e32 v142, v95, v31
	v_cndmask_b32_e32 v157, 0, v157, vcc
	v_dot4c_i32_i8_e32 v158, v68, v28
	s_cselect_b64 vcc, -1, 0
	s_cmp_gt_i32 s44, 6
	v_dot4c_i32_i8_e32 v159, v61, v29
	v_dot4c_i32_i8_e32 v160, v54, v30
	v_dot4c_i32_i8_e32 v142, v94, v30
	v_cndmask_b32_e32 v158, 0, v158, vcc
	v_dot4c_i32_i8_e32 v159, v60, v28
	s_cselect_b64 vcc, -1, 0
	s_cmp_gt_i32 s44, 7
	v_dot4c_i32_i8_e32 v160, v53, v29
	v_dot4c_i32_i8_e32 v142, v93, v29
	v_cndmask_b32_e32 v159, 0, v159, vcc
	v_dot4c_i32_i8_e32 v160, v52, v28
	s_cselect_b64 vcc, -1, 0
	v_dot4c_i32_i8_e32 v142, v92, v28
	v_permlane32_swap_b32_e32 v155, v156
	v_cndmask_b32_e32 v160, 0, v160, vcc
	s_nop 0
	v_permlane32_swap_b32_e32 v142, v154
	v_permlane32_swap_b32_e32 v157, v158
	v_permlane32_swap_b32_e32 v159, v160
	v_add_u32_e32 v142, v142, v154
	v_add_u32_e32 v154, v155, v156
	v_add_u32_e32 v155, v157, v158
	v_add_u32_e32 v156, v159, v160
	v_permlane16_swap_b32_e32 v142, v154
	s_nop 0
	v_permlane16_swap_b32_e32 v155, v156
	v_add_u32_e32 v142, v142, v154
	v_add_u32_e32 v154, v155, v156
	v_cndmask_b32_e64 v155, v154, v142, s[14:15]
	v_cndmask_b32_e64 v142, v142, v154, s[14:15]
	v_mov_b32_e32 v154, 0
	v_cmp_gt_u32_e32 vcc, s43, v144
	v_add_u32_dpp v142, v142, v155 row_ror:8 row_mask:0xf bank_mask:0xf bound_ctrl:1
	s_and_b64 s[46:47], s[16:17], vcc
	s_nop 0
	v_add_u32_dpp v142, v142, v142 quad_perm:[1,0,3,2] row_mask:0xf bank_mask:0xf bound_ctrl:1
	s_nop 1
	v_add_u32_dpp v142, v142, v142 quad_perm:[2,3,0,1] row_mask:0xf bank_mask:0xf bound_ctrl:1
	s_nop 1
	v_mov_b32_dpp v154, v142 row_half_mirror row_mask:0xf bank_mask:0xf
	s_and_saveexec_b64 s[18:19], s[46:47]
	s_cbranch_execz .LBB0_875
	v_add_u32_e32 v142, v142, v154
	v_cvt_f32_i32_e32 v142, v142
	v_lshl_add_u32 v154, s42, 2, v152
	v_mul_f32_e32 v142, 0x382aaaab, v142
	ds_write_b32 v154, v142 offset:7168

; __device__ __forceinline__ int ifold32(int a, int b) { const auto r = __builtin_amdgcn_permlane32_swap((unsigned)a, (unsigned)b, false, false); return (int)(r[0] + r[1]); }
; __device__ __forceinline__ int ifold16(int a, int b) { const auto r = __builtin_amdgcn_permlane16_swap((unsigned)a, (unsigned)b, false, false); return (int)(r[0] + r[1]); }
; template <int CTRL> __device__ __forceinline__ int idppadd(int v) { return v + __builtin_amdgcn_update_dpp(0, v, CTRL, 0xf, 0xf, false); }
.LBB0_877:
	s_andn2_b64 vcc, exec, s[18:19]
	s_cbranch_vccnz .LBB0_886
	s_cmp_gt_i32 s45, 4
	s_mov_b64 s[18:19], -1
	s_cbranch_scc0 .LBB0_882
	v_mov_b32_e32 v154, 0
	s_waitcnt vmcnt(16)
	v_dot4c_i32_i8_e32 v154, v91, v23
	v_mov_b32_e32 v155, 0
	v_dot4c_i32_i8_e32 v154, v90, v22
	v_dot4c_i32_i8_e32 v155, v87, v23
	v_mov_b32_e32 v156, 0
	s_cmp_gt_i32 s44, 1
	v_dot4c_i32_i8_e32 v154, v89, v21
	v_dot4c_i32_i8_e32 v155, v86, v22
	v_dot4c_i32_i8_e32 v156, v83, v23
	v_mov_b32_e32 v157, 0
	v_dot4c_i32_i8_e32 v154, v88, v20
	s_cselect_b64 vcc, -1, 0
	s_cmp_gt_i32 s44, 2
	v_dot4c_i32_i8_e32 v155, v85, v21
	v_dot4c_i32_i8_e32 v156, v82, v22
	v_dot4c_i32_i8_e32 v157, v79, v23
	v_mov_b32_e32 v158, 0
	v_cndmask_b32_e32 v154, 0, v154, vcc
	v_dot4c_i32_i8_e32 v155, v84, v20
	s_cselect_b64 vcc, -1, 0
	s_cmp_gt_i32 s44, 3
	v_dot4c_i32_i8_e32 v156, v81, v21
	v_dot4c_i32_i8_e32 v157, v78, v22
	v_dot4c_i32_i8_e32 v158, v71, v23
	v_mov_b32_e32 v159, 0
	v_cndmask_b32_e32 v155, 0, v155, vcc
	v_dot4c_i32_i8_e32 v156, v80, v20
	s_cselect_b64 vcc, -1, 0
	s_cmp_gt_i32 s44, 4
	v_dot4c_i32_i8_e32 v157, v77, v21
	v_dot4c_i32_i8_e32 v158, v70, v22
	v_dot4c_i32_i8_e32 v159, v63, v23
	v_mov_b32_e32 v160, 0
	v_mov_b32_e32 v142, 0
	v_cndmask_b32_e32 v156, 0, v156, vcc
	v_dot4c_i32_i8_e32 v157, v76, v20
	s_cselect_b64 vcc, -1, 0
	s_cmp_gt_i32 s44, 5
	v_dot4c_i32_i8_e32 v158, v69, v21
	v_dot4c_i32_i8_e32 v159, v62, v22
	v_dot4c_i32_i8_e32 v160, v55, v23
	s_waitcnt vmcnt(16)
	v_dot4c_i32_i8_e32 v142, v95, v23
	v_cndmask_b32_e32 v157, 0, v157, vcc
	v_dot4c_i32_i8_e32 v158, v68, v20
	s_cselect_b64 vcc, -1, 0
	s_cmp_gt_i32 s44, 6
	v_dot4c_i32_i8_e32 v159, v61, v21
	v_dot4c_i32_i8_e32 v160, v54, v22
	v_dot4c_i32_i8_e32 v142, v94, v22
	v_cndmask_b32_e32 v158, 0, v158, vcc
	v_dot4c_i32_i8_e32 v159, v60, v20
	s_cselect_b64 vcc, -1, 0
	s_cmp_gt_i32 s44, 7
	v_dot4c_i32_i8_e32 v160, v53, v21
	v_dot4c_i32_i8_e32 v142, v93, v21
	v_cndmask_b32_e32 v159, 0, v159, vcc
	v_dot4c_i32_i8_e32 v160, v52, v20
	s_cselect_b64 vcc, -1, 0
	v_dot4c_i32_i8_e32 v142, v92, v20
	v_permlane32_swap_b32_e32 v155, v156
	v_cndmask_b32_e32 v160, 0, v160, vcc
	s_nop 0
	v_permlane32_swap_b32_e32 v142, v154
	v_permlane32_swap_b32_e32 v157, v158
	v_permlane32_swap_b32_e32 v159, v160
	v_add_u32_e32 v142, v142, v154
	v_add_u32_e32 v154, v155, v156
	v_add_u32_e32 v155, v157, v158
	v_add_u32_e32 v156, v159, v160
	v_permlane16_swap_b32_e32 v142, v154
	s_nop 0
	v_permlane16_swap_b32_e32 v155, v156
	v_add_u32_e32 v142, v142, v154
	v_add_u32_e32 v154, v155, v156
	v_cndmask_b32_e64 v155, v154, v142, s[14:15]
	v_cndmask_b32_e64 v142, v142, v154, s[14:15]
	v_mov_b32_e32 v154, 0
	v_cmp_gt_u32_e32 vcc, s43, v144
	v_add_u32_dpp v142, v142, v155 row_ror:8 row_mask:0xf bank_mask:0xf bound_ctrl:1
	s_and_b64 s[46:47], s[16:17], vcc
	s_nop 0
	v_add_u32_dpp v142, v142, v142 quad_perm:[1,0,3,2] row_mask:0xf bank_mask:0xf bound_ctrl:1
	s_nop 1
	v_add_u32_dpp v142, v142, v142 quad_perm:[2,3,0,1] row_mask:0xf bank_mask:0xf bound_ctrl:1
	s_nop 1
	v_mov_b32_dpp v154, v142 row_half_mirror row_mask:0xf bank_mask:0xf
	s_and_saveexec_b64 s[18:19], s[46:47]
	s_cbranch_execz .LBB0_881
	v_add_u32_e32 v142, v142, v154
	v_cvt_f32_i32_e32 v142, v142
	v_lshl_add_u32 v154, s42, 2, v152
	v_mul_f32_e32 v142, 0x382aaaab, v142
	ds_write_b32 v154, v142 offset:6656

; __device__ __forceinline__ int ifold32(int a, int b) { const auto r = __builtin_amdgcn_permlane32_swap((unsigned)a, (unsigned)b, false, false); return (int)(r[0] + r[1]); }
; __device__ __forceinline__ int ifold16(int a, int b) { const auto r = __builtin_amdgcn_permlane16_swap((unsigned)a, (unsigned)b, false, false); return (int)(r[0] + r[1]); }
; template <int CTRL> __device__ __forceinline__ int idppadd(int v) { return v + __builtin_amdgcn_update_dpp(0, v, CTRL, 0xf, 0xf, false); }
.LBB0_882:
	s_andn2_b64 vcc, exec, s[18:19]
	s_cbranch_vccnz .LBB0_886
	v_mov_b32_e32 v154, 0
	s_waitcnt vmcnt(16)
	v_dot4c_i32_i8_e32 v154, v91, v19
	v_mov_b32_e32 v155, 0
	v_dot4c_i32_i8_e32 v154, v90, v18
	v_dot4c_i32_i8_e32 v155, v87, v19
	v_mov_b32_e32 v156, 0
	s_cmp_gt_i32 s44, 1
	v_dot4c_i32_i8_e32 v154, v89, v17
	v_dot4c_i32_i8_e32 v155, v86, v18
	v_dot4c_i32_i8_e32 v156, v83, v19
	v_mov_b32_e32 v157, 0
	v_dot4c_i32_i8_e32 v154, v88, v16
	s_cselect_b64 vcc, -1, 0
	s_cmp_gt_i32 s44, 2
	v_dot4c_i32_i8_e32 v155, v85, v17
	v_dot4c_i32_i8_e32 v156, v82, v18
	v_dot4c_i32_i8_e32 v157, v79, v19
	v_mov_b32_e32 v158, 0
	v_cndmask_b32_e32 v154, 0, v154, vcc
	v_dot4c_i32_i8_e32 v155, v84, v16
	s_cselect_b64 vcc, -1, 0
	s_cmp_gt_i32 s44, 3
	v_dot4c_i32_i8_e32 v156, v81, v17
	v_dot4c_i32_i8_e32 v157, v78, v18
	v_dot4c_i32_i8_e32 v158, v71, v19
	v_mov_b32_e32 v159, 0
	v_cndmask_b32_e32 v155, 0, v155, vcc
	v_dot4c_i32_i8_e32 v156, v80, v16
	s_cselect_b64 vcc, -1, 0
	s_cmp_gt_i32 s44, 4
	v_dot4c_i32_i8_e32 v157, v77, v17
	v_dot4c_i32_i8_e32 v158, v70, v18
	v_dot4c_i32_i8_e32 v159, v63, v19
	v_mov_b32_e32 v160, 0
	v_mov_b32_e32 v142, 0
	v_cndmask_b32_e32 v156, 0, v156, vcc
	v_dot4c_i32_i8_e32 v157, v76, v16
	s_cselect_b64 vcc, -1, 0
	s_cmp_gt_i32 s44, 5
	v_dot4c_i32_i8_e32 v158, v69, v17
	v_dot4c_i32_i8_e32 v159, v62, v18
	v_dot4c_i32_i8_e32 v160, v55, v19
	s_waitcnt vmcnt(16)
	v_dot4c_i32_i8_e32 v142, v95, v19
	v_cndmask_b32_e32 v157, 0, v157, vcc
	v_dot4c_i32_i8_e32 v158, v68, v16
	s_cselect_b64 vcc, -1, 0
	s_cmp_gt_i32 s44, 6
	v_dot4c_i32_i8_e32 v159, v61, v17
	v_dot4c_i32_i8_e32 v160, v54, v18
	v_dot4c_i32_i8_e32 v142, v94, v18
	v_cndmask_b32_e32 v158, 0, v158, vcc
	v_dot4c_i32_i8_e32 v159, v60, v16
	s_cselect_b64 vcc, -1, 0
	s_cmp_gt_i32 s44, 7
	v_dot4c_i32_i8_e32 v160, v53, v17
	v_dot4c_i32_i8_e32 v142, v93, v17
	v_cndmask_b32_e32 v159, 0, v159, vcc
	v_dot4c_i32_i8_e32 v160, v52, v16
	s_cselect_b64 vcc, -1, 0
	v_dot4c_i32_i8_e32 v142, v92, v16
	v_permlane32_swap_b32_e32 v155, v156
	v_cndmask_b32_e32 v160, 0, v160, vcc
	s_nop 0
	v_permlane32_swap_b32_e32 v142, v154
	v_permlane32_swap_b32_e32 v157, v158
	v_permlane32_swap_b32_e32 v159, v160
	v_add_u32_e32 v142, v142, v154
	v_add_u32_e32 v154, v155, v156
	v_add_u32_e32 v155, v157, v158
	v_add_u32_e32 v156, v159, v160
	v_permlane16_swap_b32_e32 v142, v154
	s_nop 0
	v_permlane16_swap_b32_e32 v155, v156
	v_add_u32_e32 v142, v142, v154
	v_add_u32_e32 v154, v155, v156
	v_cndmask_b32_e64 v155, v154, v142, s[14:15]
	v_cndmask_b32_e64 v142, v142, v154, s[14:15]
	v_mov_b32_e32 v154, 0
	v_cmp_gt_u32_e32 vcc, s43, v144
	v_add_u32_dpp v142, v142, v155 row_ror:8 row_mask:0xf bank_mask:0xf bound_ctrl:1
	s_and_b64 s[46:47], s[16:17], vcc
	s_nop 0
	v_add_u32_dpp v142, v142, v142 quad_perm:[1,0,3,2] row_mask:0xf bank_mask:0xf bound_ctrl:1
	s_nop 1
	v_add_u32_dpp v142, v142, v142 quad_perm:[2,3,0,1] row_mask:0xf bank_mask:0xf bound_ctrl:1
	s_nop 1
	v_mov_b32_dpp v154, v142 row_half_mirror row_mask:0xf bank_mask:0xf
	s_and_saveexec_b64 s[18:19], s[46:47]
	s_cbranch_execz .LBB0_885
	v_add_u32_e32 v142, v142, v154
	v_cvt_f32_i32_e32 v142, v142
	v_lshl_add_u32 v154, s42, 2, v152
	v_mul_f32_e32 v142, 0x382aaaab, v142
	ds_write_b32 v154, v142 offset:6144

; __device__ __forceinline__ int ifold32(int a, int b) { const auto r = __builtin_amdgcn_permlane32_swap((unsigned)a, (unsigned)b, false, false); return (int)(r[0] + r[1]); }
; __device__ __forceinline__ int ifold16(int a, int b) { const auto r = __builtin_amdgcn_permlane16_swap((unsigned)a, (unsigned)b, false, false); return (int)(r[0] + r[1]); }
; template <int CTRL> __device__ __forceinline__ int idppadd(int v) { return v + __builtin_amdgcn_update_dpp(0, v, CTRL, 0xf, 0xf, false); }
.LBB0_887:
	s_andn2_b64 vcc, exec, s[18:19]
	s_cbranch_vccnz .LBB0_907
	s_cmp_lt_i32 s45, 2
	s_mov_b64 s[18:19], -1
	s_cbranch_scc1 .LBB0_898
	s_cmp_gt_i32 s45, 2
	s_cbranch_scc0 .LBB0_893
	v_mov_b32_e32 v154, 0
	s_waitcnt vmcnt(16)
	v_dot4c_i32_i8_e32 v154, v91, v15
	v_mov_b32_e32 v155, 0
	v_dot4c_i32_i8_e32 v154, v90, v14
	v_dot4c_i32_i8_e32 v155, v87, v15
	v_mov_b32_e32 v156, 0
	s_cmp_gt_i32 s44, 1
	v_dot4c_i32_i8_e32 v154, v89, v13
	v_dot4c_i32_i8_e32 v155, v86, v14
	v_dot4c_i32_i8_e32 v156, v83, v15
	v_mov_b32_e32 v157, 0
	v_dot4c_i32_i8_e32 v154, v88, v12
	s_cselect_b64 vcc, -1, 0
	s_cmp_gt_i32 s44, 2
	v_dot4c_i32_i8_e32 v155, v85, v13
	v_dot4c_i32_i8_e32 v156, v82, v14
	v_dot4c_i32_i8_e32 v157, v79, v15
	v_mov_b32_e32 v158, 0
	v_cndmask_b32_e32 v154, 0, v154, vcc
	v_dot4c_i32_i8_e32 v155, v84, v12
	s_cselect_b64 vcc, -1, 0
	s_cmp_gt_i32 s44, 3
	v_dot4c_i32_i8_e32 v156, v81, v13
	v_dot4c_i32_i8_e32 v157, v78, v14
	v_dot4c_i32_i8_e32 v158, v71, v15
	v_mov_b32_e32 v159, 0
	v_cndmask_b32_e32 v155, 0, v155, vcc
	v_dot4c_i32_i8_e32 v156, v80, v12
	s_cselect_b64 vcc, -1, 0
	s_cmp_gt_i32 s44, 4
	v_dot4c_i32_i8_e32 v157, v77, v13
	v_dot4c_i32_i8_e32 v158, v70, v14
	v_dot4c_i32_i8_e32 v159, v63, v15
	v_mov_b32_e32 v160, 0
	v_mov_b32_e32 v142, 0
	v_cndmask_b32_e32 v156, 0, v156, vcc
	v_dot4c_i32_i8_e32 v157, v76, v12
	s_cselect_b64 vcc, -1, 0
	s_cmp_gt_i32 s44, 5
	v_dot4c_i32_i8_e32 v158, v69, v13
	v_dot4c_i32_i8_e32 v159, v62, v14
	v_dot4c_i32_i8_e32 v160, v55, v15
	s_waitcnt vmcnt(16)
	v_dot4c_i32_i8_e32 v142, v95, v15
	v_cndmask_b32_e32 v157, 0, v157, vcc
	v_dot4c_i32_i8_e32 v158, v68, v12
	s_cselect_b64 vcc, -1, 0
	s_cmp_gt_i32 s44, 6
	v_dot4c_i32_i8_e32 v159, v61, v13
	v_dot4c_i32_i8_e32 v160, v54, v14
	v_dot4c_i32_i8_e32 v142, v94, v14
	v_cndmask_b32_e32 v158, 0, v158, vcc
	v_dot4c_i32_i8_e32 v159, v60, v12
	s_cselect_b64 vcc, -1, 0
	s_cmp_gt_i32 s44, 7
	v_dot4c_i32_i8_e32 v160, v53, v13
	v_dot4c_i32_i8_e32 v142, v93, v13
	v_cndmask_b32_e32 v159, 0, v159, vcc
	v_dot4c_i32_i8_e32 v160, v52, v12
	s_cselect_b64 vcc, -1, 0
	v_dot4c_i32_i8_e32 v142, v92, v12
	v_permlane32_swap_b32_e32 v155, v156
	v_cndmask_b32_e32 v160, 0, v160, vcc
	s_nop 0
	v_permlane32_swap_b32_e32 v142, v154
	v_permlane32_swap_b32_e32 v157, v158
	v_permlane32_swap_b32_e32 v159, v160
	v_add_u32_e32 v142, v142, v154
	v_add_u32_e32 v154, v155, v156
	v_add_u32_e32 v155, v157, v158
	v_add_u32_e32 v156, v159, v160
	v_permlane16_swap_b32_e32 v142, v154
	s_nop 0
	v_permlane16_swap_b32_e32 v155, v156
	v_add_u32_e32 v142, v142, v154
	v_add_u32_e32 v154, v155, v156
	v_cndmask_b32_e64 v155, v154, v142, s[14:15]
	v_cndmask_b32_e64 v142, v142, v154, s[14:15]
	v_mov_b32_e32 v154, 0
	v_cmp_gt_u32_e32 vcc, s43, v144
	v_add_u32_dpp v142, v142, v155 row_ror:8 row_mask:0xf bank_mask:0xf bound_ctrl:1
	s_and_b64 s[46:47], s[16:17], vcc
	s_nop 0
	v_add_u32_dpp v142, v142, v142 quad_perm:[1,0,3,2] row_mask:0xf bank_mask:0xf bound_ctrl:1
	s_nop 1
	v_add_u32_dpp v142, v142, v142 quad_perm:[2,3,0,1] row_mask:0xf bank_mask:0xf bound_ctrl:1
	s_nop 1
	v_mov_b32_dpp v154, v142 row_half_mirror row_mask:0xf bank_mask:0xf
	s_and_saveexec_b64 s[18:19], s[46:47]
	s_cbranch_execz .LBB0_892
	v_add_u32_e32 v142, v142, v154
	v_cvt_f32_i32_e32 v142, v142
	v_lshl_add_u32 v154, s42, 2, v152
	v_mul_f32_e32 v142, 0x382aaaab, v142
	ds_write_b32 v154, v142 offset:5632

; __device__ __forceinline__ int ifold32(int a, int b) { const auto r = __builtin_amdgcn_permlane32_swap((unsigned)a, (unsigned)b, false, false); return (int)(r[0] + r[1]); }
; __device__ __forceinline__ int ifold16(int a, int b) { const auto r = __builtin_amdgcn_permlane16_swap((unsigned)a, (unsigned)b, false, false); return (int)(r[0] + r[1]); }
; template <int CTRL> __device__ __forceinline__ int idppadd(int v) { return v + __builtin_amdgcn_update_dpp(0, v, CTRL, 0xf, 0xf, false); }
.LBB0_893:
	s_andn2_b64 vcc, exec, s[18:19]
	s_cbranch_vccnz .LBB0_897
	v_mov_b32_e32 v154, 0
	s_waitcnt vmcnt(16)
	v_dot4c_i32_i8_e32 v154, v91, v11
	v_mov_b32_e32 v155, 0
	v_dot4c_i32_i8_e32 v154, v90, v10
	v_dot4c_i32_i8_e32 v155, v87, v11
	v_mov_b32_e32 v156, 0
	s_cmp_gt_i32 s44, 1
	v_dot4c_i32_i8_e32 v154, v89, v9
	v_dot4c_i32_i8_e32 v155, v86, v10
	v_dot4c_i32_i8_e32 v156, v83, v11
	v_mov_b32_e32 v157, 0
	v_dot4c_i32_i8_e32 v154, v88, v8
	s_cselect_b64 vcc, -1, 0
	s_cmp_gt_i32 s44, 2
	v_dot4c_i32_i8_e32 v155, v85, v9
	v_dot4c_i32_i8_e32 v156, v82, v10
	v_dot4c_i32_i8_e32 v157, v79, v11
	v_mov_b32_e32 v158, 0
	v_cndmask_b32_e32 v154, 0, v154, vcc
	v_dot4c_i32_i8_e32 v155, v84, v8
	s_cselect_b64 vcc, -1, 0
	s_cmp_gt_i32 s44, 3
	v_dot4c_i32_i8_e32 v156, v81, v9
	v_dot4c_i32_i8_e32 v157, v78, v10
	v_dot4c_i32_i8_e32 v158, v71, v11
	v_mov_b32_e32 v159, 0
	v_cndmask_b32_e32 v155, 0, v155, vcc
	v_dot4c_i32_i8_e32 v156, v80, v8
	s_cselect_b64 vcc, -1, 0
	s_cmp_gt_i32 s44, 4
	v_dot4c_i32_i8_e32 v157, v77, v9
	v_dot4c_i32_i8_e32 v158, v70, v10
	v_dot4c_i32_i8_e32 v159, v63, v11
	v_mov_b32_e32 v160, 0
	v_mov_b32_e32 v142, 0
	v_cndmask_b32_e32 v156, 0, v156, vcc
	v_dot4c_i32_i8_e32 v157, v76, v8
	s_cselect_b64 vcc, -1, 0
	s_cmp_gt_i32 s44, 5
	v_dot4c_i32_i8_e32 v158, v69, v9
	v_dot4c_i32_i8_e32 v159, v62, v10
	v_dot4c_i32_i8_e32 v160, v55, v11
	s_waitcnt vmcnt(16)
	v_dot4c_i32_i8_e32 v142, v95, v11
	v_cndmask_b32_e32 v157, 0, v157, vcc
	v_dot4c_i32_i8_e32 v158, v68, v8
	s_cselect_b64 vcc, -1, 0
	s_cmp_gt_i32 s44, 6
	v_dot4c_i32_i8_e32 v159, v61, v9
	v_dot4c_i32_i8_e32 v160, v54, v10
	v_dot4c_i32_i8_e32 v142, v94, v10
	v_cndmask_b32_e32 v158, 0, v158, vcc
	v_dot4c_i32_i8_e32 v159, v60, v8
	s_cselect_b64 vcc, -1, 0
	s_cmp_gt_i32 s44, 7
	v_dot4c_i32_i8_e32 v160, v53, v9
	v_dot4c_i32_i8_e32 v142, v93, v9
	v_cndmask_b32_e32 v159, 0, v159, vcc
	v_dot4c_i32_i8_e32 v160, v52, v8
	s_cselect_b64 vcc, -1, 0
	v_dot4c_i32_i8_e32 v142, v92, v8
	v_permlane32_swap_b32_e32 v155, v156
	v_cndmask_b32_e32 v160, 0, v160, vcc
	s_nop 0
	v_permlane32_swap_b32_e32 v142, v154
	v_permlane32_swap_b32_e32 v157, v158
	v_permlane32_swap_b32_e32 v159, v160
	v_add_u32_e32 v142, v142, v154
	v_add_u32_e32 v154, v155, v156
	v_add_u32_e32 v155, v157, v158
	v_add_u32_e32 v156, v159, v160
	v_permlane16_swap_b32_e32 v142, v154
	s_nop 0
	v_permlane16_swap_b32_e32 v155, v156
	v_add_u32_e32 v142, v142, v154
	v_add_u32_e32 v154, v155, v156
	v_cndmask_b32_e64 v155, v154, v142, s[14:15]
	v_cndmask_b32_e64 v142, v142, v154, s[14:15]
	v_mov_b32_e32 v154, 0
	v_cmp_gt_u32_e32 vcc, s43, v144
	v_add_u32_dpp v142, v142, v155 row_ror:8 row_mask:0xf bank_mask:0xf bound_ctrl:1
	s_and_b64 s[46:47], s[16:17], vcc
	s_nop 0
	v_add_u32_dpp v142, v142, v142 quad_perm:[1,0,3,2] row_mask:0xf bank_mask:0xf bound_ctrl:1
	s_nop 1
	v_add_u32_dpp v142, v142, v142 quad_perm:[2,3,0,1] row_mask:0xf bank_mask:0xf bound_ctrl:1
	s_nop 1
	v_mov_b32_dpp v154, v142 row_half_mirror row_mask:0xf bank_mask:0xf
	s_and_saveexec_b64 s[18:19], s[46:47]
	s_cbranch_execz .LBB0_896
	v_add_u32_e32 v142, v142, v154
	v_cvt_f32_i32_e32 v142, v142
	v_lshl_add_u32 v154, s42, 2, v152
	v_mul_f32_e32 v142, 0x382aaaab, v142
	ds_write_b32 v154, v142 offset:5120

; __device__ __forceinline__ int ifold32(int a, int b) { const auto r = __builtin_amdgcn_permlane32_swap((unsigned)a, (unsigned)b, false, false); return (int)(r[0] + r[1]); }
; __device__ __forceinline__ int ifold16(int a, int b) { const auto r = __builtin_amdgcn_permlane16_swap((unsigned)a, (unsigned)b, false, false); return (int)(r[0] + r[1]); }
; template <int CTRL> __device__ __forceinline__ int idppadd(int v) { return v + __builtin_amdgcn_update_dpp(0, v, CTRL, 0xf, 0xf, false); }
.LBB0_898:
	s_andn2_b64 vcc, exec, s[18:19]
	s_cbranch_vccnz .LBB0_907
	s_mov_b64 s[18:19], -1
	s_cmp_eq_u32 s45, 1
	v_cmp_gt_u32_e32 vcc, s43, v144
	s_cbranch_scc1 .LBB0_903
	v_mov_b32_e32 v154, 0
	s_waitcnt vmcnt(16)
	v_dot4c_i32_i8_e32 v154, v91, v3
	v_mov_b32_e32 v155, 0
	v_dot4c_i32_i8_e32 v154, v90, v2
	v_dot4c_i32_i8_e32 v155, v87, v3
	v_mov_b32_e32 v156, 0
	s_cmp_gt_i32 s44, 1
	v_dot4c_i32_i8_e32 v154, v89, v1
	v_dot4c_i32_i8_e32 v155, v86, v2
	v_dot4c_i32_i8_e32 v156, v83, v3
	v_mov_b32_e32 v157, 0
	v_dot4c_i32_i8_e32 v154, v88, v0
	s_cselect_b64 s[18:19], -1, 0
	s_cmp_gt_i32 s44, 2
	v_dot4c_i32_i8_e32 v155, v85, v1
	v_dot4c_i32_i8_e32 v156, v82, v2
	v_dot4c_i32_i8_e32 v157, v79, v3
	v_mov_b32_e32 v158, 0
	v_cndmask_b32_e64 v154, 0, v154, s[18:19]
	v_dot4c_i32_i8_e32 v155, v84, v0
	s_cselect_b64 s[18:19], -1, 0
	s_cmp_gt_i32 s44, 3
	v_dot4c_i32_i8_e32 v156, v81, v1
	v_dot4c_i32_i8_e32 v157, v78, v2
	v_dot4c_i32_i8_e32 v158, v71, v3
	v_mov_b32_e32 v159, 0
	v_cndmask_b32_e64 v155, 0, v155, s[18:19]
	v_dot4c_i32_i8_e32 v156, v80, v0
	s_cselect_b64 s[18:19], -1, 0
	s_cmp_gt_i32 s44, 4
	v_dot4c_i32_i8_e32 v157, v77, v1
	v_dot4c_i32_i8_e32 v158, v70, v2
	v_dot4c_i32_i8_e32 v159, v63, v3
	v_mov_b32_e32 v160, 0
	v_mov_b32_e32 v142, 0
	v_cndmask_b32_e64 v156, 0, v156, s[18:19]
	v_dot4c_i32_i8_e32 v157, v76, v0
	s_cselect_b64 s[18:19], -1, 0
	s_cmp_gt_i32 s44, 5
	v_dot4c_i32_i8_e32 v158, v69, v1
	v_dot4c_i32_i8_e32 v159, v62, v2
	v_dot4c_i32_i8_e32 v160, v55, v3
	s_waitcnt vmcnt(16)
	v_dot4c_i32_i8_e32 v142, v95, v3
	v_cndmask_b32_e64 v157, 0, v157, s[18:19]
	v_dot4c_i32_i8_e32 v158, v68, v0
	s_cselect_b64 s[18:19], -1, 0
	s_cmp_gt_i32 s44, 6
	v_dot4c_i32_i8_e32 v159, v61, v1
	v_dot4c_i32_i8_e32 v160, v54, v2
	v_dot4c_i32_i8_e32 v142, v94, v2
	v_cndmask_b32_e64 v158, 0, v158, s[18:19]
	v_dot4c_i32_i8_e32 v159, v60, v0
	s_cselect_b64 s[18:19], -1, 0
	s_cmp_gt_i32 s44, 7
	v_dot4c_i32_i8_e32 v160, v53, v1
	v_dot4c_i32_i8_e32 v142, v93, v1
	v_cndmask_b32_e64 v159, 0, v159, s[18:19]
	v_dot4c_i32_i8_e32 v160, v52, v0
	s_cselect_b64 s[18:19], -1, 0
	v_dot4c_i32_i8_e32 v142, v92, v0
	v_permlane32_swap_b32_e32 v155, v156
	v_cndmask_b32_e64 v160, 0, v160, s[18:19]
	s_nop 0
	v_permlane32_swap_b32_e32 v142, v154
	v_permlane32_swap_b32_e32 v157, v158
	v_permlane32_swap_b32_e32 v159, v160
	v_add_u32_e32 v142, v142, v154
	v_add_u32_e32 v154, v155, v156
	v_add_u32_e32 v155, v157, v158
	v_add_u32_e32 v156, v159, v160
	v_permlane16_swap_b32_e32 v142, v154
	s_nop 0
	v_permlane16_swap_b32_e32 v155, v156
	v_add_u32_e32 v142, v142, v154
	v_add_u32_e32 v154, v155, v156
	v_cndmask_b32_e64 v155, v154, v142, s[14:15]
	v_cndmask_b32_e64 v142, v142, v154, s[14:15]
	v_mov_b32_e32 v154, 0
	s_and_b64 s[46:47], s[16:17], vcc
	v_add_u32_dpp v142, v142, v155 row_ror:8 row_mask:0xf bank_mask:0xf bound_ctrl:1
	s_nop 1
	v_add_u32_dpp v142, v142, v142 quad_perm:[1,0,3,2] row_mask:0xf bank_mask:0xf bound_ctrl:1
	s_nop 1
	v_add_u32_dpp v142, v142, v142 quad_perm:[2,3,0,1] row_mask:0xf bank_mask:0xf bound_ctrl:1
	s_nop 1
	v_mov_b32_dpp v154, v142 row_half_mirror row_mask:0xf bank_mask:0xf
	s_and_saveexec_b64 s[18:19], s[46:47]
	s_cbranch_execz .LBB0_902
	v_add_u32_e32 v142, v142, v154
	v_cvt_f32_i32_e32 v142, v142
	v_lshl_add_u32 v154, s42, 2, v152
	v_mul_f32_e32 v142, 0x382aaaab, v142
	ds_write_b32 v154, v142 offset:4096

; __device__ __forceinline__ int ifold32(int a, int b) { const auto r = __builtin_amdgcn_permlane32_swap((unsigned)a, (unsigned)b, false, false); return (int)(r[0] + r[1]); }
; __device__ __forceinline__ int ifold16(int a, int b) { const auto r = __builtin_amdgcn_permlane16_swap((unsigned)a, (unsigned)b, false, false); return (int)(r[0] + r[1]); }
; template <int CTRL> __device__ __forceinline__ int idppadd(int v) { return v + __builtin_amdgcn_update_dpp(0, v, CTRL, 0xf, 0xf, false); }
.LBB0_903:
	s_andn2_b64 vcc, exec, s[18:19]
	s_cbranch_vccnz .LBB0_907
	v_mov_b32_e32 v142, 0
	s_waitcnt vmcnt(16)
	v_dot4c_i32_i8_e32 v142, v95, v7
	v_dot4c_i32_i8_e32 v142, v94, v6
	v_dot4c_i32_i8_e32 v142, v93, v5
	v_dot4c_i32_i8_e32 v142, v92, v4
	v_mov_b32_e32 v92, 0
	v_dot4c_i32_i8_e32 v92, v91, v7
	v_dot4c_i32_i8_e32 v92, v90, v6
	v_dot4c_i32_i8_e32 v92, v89, v5
	v_mov_b32_e32 v89, 0
	v_dot4c_i32_i8_e32 v89, v87, v7
	v_dot4c_i32_i8_e32 v89, v86, v6
	v_dot4c_i32_i8_e32 v89, v85, v5
	v_mov_b32_e32 v85, 0
	v_dot4c_i32_i8_e32 v85, v83, v7
	v_dot4c_i32_i8_e32 v85, v82, v6
	v_dot4c_i32_i8_e32 v85, v81, v5
	v_mov_b32_e32 v81, 0
	v_dot4c_i32_i8_e32 v81, v79, v7
	v_dot4c_i32_i8_e32 v81, v78, v6
	v_dot4c_i32_i8_e32 v81, v77, v5
	v_mov_b32_e32 v77, 0
	v_dot4c_i32_i8_e32 v77, v71, v7
	v_dot4c_i32_i8_e32 v77, v70, v6
	s_cmp_gt_i32 s44, 1
	v_dot4c_i32_i8_e32 v77, v69, v5
	v_mov_b32_e32 v69, 0
	v_dot4c_i32_i8_e32 v92, v88, v4
	s_cselect_b64 vcc, -1, 0
	s_cmp_gt_i32 s44, 2
	v_dot4c_i32_i8_e32 v69, v63, v7
	v_cndmask_b32_e32 v88, 0, v92, vcc
	v_dot4c_i32_i8_e32 v89, v84, v4
	s_cselect_b64 vcc, -1, 0
	s_cmp_gt_i32 s44, 3
	v_dot4c_i32_i8_e32 v69, v62, v6
	v_cndmask_b32_e32 v84, 0, v89, vcc
	v_dot4c_i32_i8_e32 v85, v80, v4
	s_cselect_b64 vcc, -1, 0
	s_cmp_gt_i32 s44, 4
	v_dot4c_i32_i8_e32 v69, v61, v5
	v_mov_b32_e32 v61, 0
	v_cndmask_b32_e32 v80, 0, v85, vcc
	v_dot4c_i32_i8_e32 v81, v76, v4
	s_cselect_b64 vcc, -1, 0
	s_cmp_gt_i32 s44, 5
	v_dot4c_i32_i8_e32 v61, v55, v7
	v_cndmask_b32_e32 v76, 0, v81, vcc
	v_dot4c_i32_i8_e32 v77, v68, v4
	s_cselect_b64 vcc, -1, 0
	s_cmp_gt_i32 s44, 6
	v_dot4c_i32_i8_e32 v61, v54, v6
	v_cndmask_b32_e32 v68, 0, v77, vcc
	v_dot4c_i32_i8_e32 v69, v60, v4
	s_cselect_b64 vcc, -1, 0
	s_cmp_gt_i32 s44, 7
	v_dot4c_i32_i8_e32 v61, v53, v5
	v_cndmask_b32_e32 v60, 0, v69, vcc
	v_dot4c_i32_i8_e32 v61, v52, v4
	s_cselect_b64 vcc, -1, 0
	v_permlane32_swap_b32_e32 v142, v88
	s_nop 0
	v_cndmask_b32_e32 v52, 0, v61, vcc
	v_permlane32_swap_b32_e32 v84, v80
	v_permlane32_swap_b32_e32 v76, v68
	v_permlane32_swap_b32_e32 v60, v52
	v_add_u32_e32 v53, v142, v88
	v_add_u32_e32 v54, v84, v80
	v_add_u32_e32 v55, v76, v68
	v_add_u32_e32 v52, v60, v52
	v_permlane16_swap_b32_e32 v53, v54
	s_nop 0
	v_permlane16_swap_b32_e32 v55, v52
	v_add_u32_e32 v53, v53, v54
	v_add_u32_e32 v52, v55, v52
	v_cndmask_b32_e64 v54, v52, v53, s[14:15]
	v_cndmask_b32_e64 v52, v53, v52, s[14:15]
	v_mov_b32_e32 v53, 0
	v_cmp_gt_u32_e32 vcc, s43, v144
	v_add_u32_dpp v52, v52, v54 row_ror:8 row_mask:0xf bank_mask:0xf bound_ctrl:1
	s_and_b64 s[44:45], s[16:17], vcc
	s_nop 0
	v_add_u32_dpp v52, v52, v52 quad_perm:[1,0,3,2] row_mask:0xf bank_mask:0xf bound_ctrl:1
	s_nop 1
	v_add_u32_dpp v52, v52, v52 quad_perm:[2,3,0,1] row_mask:0xf bank_mask:0xf bound_ctrl:1
	s_nop 1
	v_mov_b32_dpp v53, v52 row_half_mirror row_mask:0xf bank_mask:0xf
	s_and_saveexec_b64 s[18:19], s[44:45]
	s_cbranch_execz .LBB0_906
	v_add_u32_e32 v52, v52, v53
	v_cvt_f32_i32_e32 v52, v52
	v_lshl_add_u32 v53, s42, 2, v152
	v_mul_f32_e32 v52, 0x382aaaab, v52
	ds_write_b32 v53, v52 offset:4608
